# union 8: router-logit loop software pipelined (next k-step's loads in flight, two register sets)
# speedup vs baseline: 1.0048x; 1.0048x over previous
.LBB0_822:
	s_mov_b64 s[54:55], exec
	v_readlane_b32 s56, v243, 24
	v_readlane_b32 s57, v243, 25
	s_and_b64 s[56:57], s[54:55], s[56:57]
	s_mov_b64 exec, s[56:57]
	ds_write_b32 v154, v133 offset:512
	s_or_b64 exec, exec, s[54:55]
	s_ashr_i32 s3, s2, 31
	s_lshr_b32 s54, s3, 25
	s_add_i32 s54, s2, s54
	s_ashr_i32 s56, s54, 7
	s_mul_i32 s54, s56, 0x3000
	s_ashr_i32 s55, s54, 31
	s_lshl_b64 s[54:55], s[54:55], 2
	v_readlane_b32 s57, v243, 26
	s_add_u32 s54, s57, s54
	v_readlane_b32 s57, v243, 27
	s_addc_u32 s55, s57, s55
	v_lshl_add_u64 v[10:11], v[130:131], 2, s[54:55]
	s_movk_i32 s54, 0x6000
	v_add_co_u32_e32 v6, vcc, s54, v10
	s_mov_b32 s54, 0x8000
	s_nop 0
	v_addc_co_u32_e32 v7, vcc, 0, v11, vcc
	v_add_co_u32_e32 v10, vcc, s54, v10
	v_ashrrev_i32_e32 v151, 31, v150
	s_nop 0
	v_addc_co_u32_e32 v11, vcc, 0, v11, vcc
	v_lshlrev_b64 v[2:3], 13, v[150:151]
	global_load_dwordx4 v[6:9], v[6:7], off
	v_lshl_add_u64 v[46:47], v[148:149], 0, v[2:3]
	global_load_dwordx4 v[10:13], v[10:11], off
	s_lshl_b32 s65, s56, 6
	global_load_dwordx4 v[2:5], v[134:135], off
	v_readlane_b32 s56, v242, 20
	v_readlane_b32 s58, v242, 22
	v_readlane_b32 s59, v242, 23
	s_mov_b64 s[54:55], 0
	v_readlane_b32 s57, v242, 21
	s_waitcnt vmcnt(1)
	v_pk_add_f32 v[12:13], v[12:13], 1.0 op_sel_hi:[1,0]
	v_pk_add_f32 v[10:11], v[10:11], 1.0 op_sel_hi:[1,0]
	s_waitcnt vmcnt(0)
	v_pk_mul_f32 v[4:5], v[4:5], v[12:13]
	v_pk_mul_f32 v[2:3], v[2:3], v[10:11]
	ds_write_b128 v155, v[2:5]
	ds_write_b128 v156, v[6:9]
	v_or_b32_e32 v2, s65, v157
	v_ashrrev_i32_e32 v3, 31, v2
	v_lshlrev_b64 v[2:3], 11, v[2:3]
	v_lshl_add_u64 v[2:3], v[146:147], 0, v[2:3]
	v_lshl_add_u64 v[48:49], v[2:3], 1, s[58:59]
	v_mov_b32_e32 v2, 0
	v_mov_b32_e32 v3, v2
	v_mov_b32_e32 v4, v2
	v_mov_b32_e32 v5, v2
	v_mov_b32_e32 v6, v2
	v_mov_b32_e32 v7, v2
	v_mov_b32_e32 v8, v2
	v_mov_b32_e32 v9, v2
	v_mov_b32_e32 v10, v2
	v_mov_b32_e32 v11, v2
	v_mov_b32_e32 v12, v2
	v_mov_b32_e32 v13, v2
	v_mov_b32_e32 v14, v2
	v_mov_b32_e32 v15, v2
	v_mov_b32_e32 v16, v2
	v_mov_b32_e32 v17, v2
	v_mov_b32_e32 v18, v2
	v_mov_b32_e32 v19, v2
	v_mov_b32_e32 v20, v2
	v_mov_b32_e32 v21, v2
	v_mov_b32_e32 v22, v2
	v_mov_b32_e32 v23, v2
	v_mov_b32_e32 v24, v2
	v_mov_b32_e32 v25, v2
	v_mov_b32_e32 v26, v2
	v_mov_b32_e32 v27, v2
	v_mov_b32_e32 v28, v2
	v_mov_b32_e32 v29, v2
	v_mov_b32_e32 v30, v2
	v_mov_b32_e32 v31, v2
	v_mov_b32_e32 v32, v2
	v_mov_b32_e32 v33, v2
	s_mov_b32 s60, 0x39e00000
	s_mov_b32 s61, 0
	v_lshl_add_u64 v[100:101], v[48:49], 0, s[60:61]
	s_mov_b32 s60, 0x39e80000
	s_mov_b32 s61, 0
	v_lshl_add_u64 v[102:103], v[48:49], 0, s[60:61]
	s_mov_b32 s60, 0x39e20000
	s_mov_b32 s61, 0
	v_lshl_add_u64 v[104:105], v[48:49], 0, s[60:61]
	s_mov_b32 s60, 0x39ea0000
	s_mov_b32 s61, 0
	v_lshl_add_u64 v[106:107], v[48:49], 0, s[60:61]
	s_mov_b64 s[60:61], 0x80
	s_mov_b64 s[56:57], 0x100
	global_load_dwordx4 v[34:37], v[46:47], off offset:-112
	global_load_dwordx4 v[38:41], v[46:47], off offset:-128
	global_load_dwordx4 v[54:57], v[100:101], off
	global_load_dwordx4 v[62:65], v[104:105], off
	global_load_dwordx4 v[58:61], v[102:103], off
	global_load_dwordx4 v[66:69], v[106:107], off
.LBB0_825:
	global_load_dwordx4 v[76:79], v[46:47], off offset:-48
	global_load_dwordx4 v[80:83], v[46:47], off offset:-64
	global_load_dwordx4 v[84:87], v[100:101], off offset:32
	global_load_dwordx4 v[92:95], v[104:105], off offset:32
	global_load_dwordx4 v[88:91], v[102:103], off offset:32
	global_load_dwordx4 v[96:99], v[106:107], off offset:32
	s_waitcnt vmcnt(11)
	v_cvt_pk_bf16_f32 v72, v34, v35
	s_waitcnt vmcnt(10)
	v_cvt_pk_bf16_f32 v70, v38, v39
	v_cvt_pk_bf16_f32 v71, v40, v41
	v_cvt_pk_bf16_f32 v73, v36, v37
	v_lshlrev_b32_e32 v74, 16, v70
	v_and_b32_e32 v75, 0xffff0000, v70
	s_waitcnt vmcnt(9)
	v_mfma_f32_32x32x16_bf16 v[2:17], v[54:57], v[70:73], v[2:17]
	v_add_f32_e64 v38, v38, -v74
	v_add_f32_e64 v39, v39, -v75
	v_lshlrev_b32_e32 v74, 16, v71
	v_and_b32_e32 v75, 0xffff0000, v71
	v_add_f32_e64 v40, v40, -v74
	v_add_f32_e64 v41, v41, -v75
	v_cvt_pk_bf16_f32 v38, v38, v39
	v_cvt_pk_bf16_f32 v39, v40, v41
	v_lshlrev_b32_e32 v40, 16, v72
	s_waitcnt vmcnt(8)
	v_mfma_f32_32x32x16_bf16 v[18:33], v[62:65], v[70:73], v[18:33]
	v_and_b32_e32 v41, 0xffff0000, v72
	v_add_f32_e64 v34, v34, -v40
	v_add_f32_e64 v35, v35, -v41
	v_cvt_pk_bf16_f32 v40, v34, v35
	v_lshlrev_b32_e32 v34, 16, v73
	v_and_b32_e32 v35, 0xffff0000, v73
	v_pk_add_f32 v[34:35], v[36:37], v[34:35] neg_lo:[0,1] neg_hi:[0,1]
	s_waitcnt vmcnt(7)
	v_mfma_f32_32x32x16_bf16 v[2:17], v[58:61], v[70:73], v[2:17]
	v_cvt_pk_bf16_f32 v41, v34, v35
	s_waitcnt vmcnt(6)
	v_mfma_f32_32x32x16_bf16 v[18:33], v[66:69], v[70:73], v[18:33]
	v_mfma_f32_32x32x16_bf16 v[2:17], v[54:57], v[38:41], v[2:17]
	v_mfma_f32_32x32x16_bf16 v[18:33], v[62:65], v[38:41], v[18:33]
	global_load_dwordx4 v[34:37], v[46:47], off offset:16
	global_load_dwordx4 v[38:41], v[46:47], off
	global_load_dwordx4 v[54:57], v[100:101], off offset:64
	global_load_dwordx4 v[62:65], v[104:105], off offset:64
	global_load_dwordx4 v[58:61], v[102:103], off offset:64
	global_load_dwordx4 v[66:69], v[106:107], off offset:64
	s_waitcnt vmcnt(11)
	v_cvt_pk_bf16_f32 v72, v76, v77
	s_waitcnt vmcnt(10)
	v_cvt_pk_bf16_f32 v70, v80, v81
	v_cvt_pk_bf16_f32 v71, v82, v83
	v_cvt_pk_bf16_f32 v73, v78, v79
	v_lshlrev_b32_e32 v74, 16, v70
	v_and_b32_e32 v75, 0xffff0000, v70
	s_waitcnt vmcnt(9)
	v_mfma_f32_32x32x16_bf16 v[2:17], v[84:87], v[70:73], v[2:17]
	v_add_f32_e64 v80, v80, -v74
	v_add_f32_e64 v81, v81, -v75
	v_lshlrev_b32_e32 v74, 16, v71
	v_and_b32_e32 v75, 0xffff0000, v71
	v_add_f32_e64 v82, v82, -v74
	v_add_f32_e64 v83, v83, -v75
	v_cvt_pk_bf16_f32 v80, v80, v81
	v_cvt_pk_bf16_f32 v81, v82, v83
	v_lshlrev_b32_e32 v82, 16, v72
	s_waitcnt vmcnt(8)
	v_mfma_f32_32x32x16_bf16 v[18:33], v[92:95], v[70:73], v[18:33]
	v_and_b32_e32 v83, 0xffff0000, v72
	v_add_f32_e64 v76, v76, -v82
	v_add_f32_e64 v77, v77, -v83
	v_cvt_pk_bf16_f32 v82, v76, v77
	v_lshlrev_b32_e32 v76, 16, v73
	v_and_b32_e32 v77, 0xffff0000, v73
	v_pk_add_f32 v[76:77], v[78:79], v[76:77] neg_lo:[0,1] neg_hi:[0,1]
	s_waitcnt vmcnt(7)
	v_mfma_f32_32x32x16_bf16 v[2:17], v[88:91], v[70:73], v[2:17]
	v_cvt_pk_bf16_f32 v83, v76, v77
	s_waitcnt vmcnt(6)
	v_mfma_f32_32x32x16_bf16 v[18:33], v[96:99], v[70:73], v[18:33]
	v_mfma_f32_32x32x16_bf16 v[2:17], v[84:87], v[80:83], v[2:17]
	v_mfma_f32_32x32x16_bf16 v[18:33], v[92:95], v[80:83], v[18:33]
	global_load_dwordx4 v[76:79], v[46:47], off offset:80
	global_load_dwordx4 v[80:83], v[46:47], off offset:64
	global_load_dwordx4 v[84:87], v[100:101], off offset:96
	global_load_dwordx4 v[92:95], v[104:105], off offset:96
	global_load_dwordx4 v[88:91], v[102:103], off offset:96
	global_load_dwordx4 v[96:99], v[106:107], off offset:96
	s_waitcnt vmcnt(11)
	v_cvt_pk_bf16_f32 v72, v34, v35
	s_waitcnt vmcnt(10)
	v_cvt_pk_bf16_f32 v70, v38, v39
	v_cvt_pk_bf16_f32 v71, v40, v41
	v_cvt_pk_bf16_f32 v73, v36, v37
	v_lshlrev_b32_e32 v74, 16, v70
	v_and_b32_e32 v75, 0xffff0000, v70
	s_waitcnt vmcnt(9)
	v_mfma_f32_32x32x16_bf16 v[2:17], v[54:57], v[70:73], v[2:17]
	v_add_f32_e64 v38, v38, -v74
	v_add_f32_e64 v39, v39, -v75
	v_lshlrev_b32_e32 v74, 16, v71
	v_and_b32_e32 v75, 0xffff0000, v71
	v_add_f32_e64 v40, v40, -v74
	v_add_f32_e64 v41, v41, -v75
	v_cvt_pk_bf16_f32 v38, v38, v39
	v_cvt_pk_bf16_f32 v39, v40, v41
	v_lshlrev_b32_e32 v40, 16, v72
	s_waitcnt vmcnt(8)
	v_mfma_f32_32x32x16_bf16 v[18:33], v[62:65], v[70:73], v[18:33]
	v_and_b32_e32 v41, 0xffff0000, v72
	v_add_f32_e64 v34, v34, -v40
	v_add_f32_e64 v35, v35, -v41
	v_cvt_pk_bf16_f32 v40, v34, v35
	v_lshlrev_b32_e32 v34, 16, v73
	v_and_b32_e32 v35, 0xffff0000, v73
	v_pk_add_f32 v[34:35], v[36:37], v[34:35] neg_lo:[0,1] neg_hi:[0,1]
	s_waitcnt vmcnt(7)
	v_mfma_f32_32x32x16_bf16 v[2:17], v[58:61], v[70:73], v[2:17]
	v_cvt_pk_bf16_f32 v41, v34, v35
	s_waitcnt vmcnt(6)
	v_mfma_f32_32x32x16_bf16 v[18:33], v[66:69], v[70:73], v[18:33]
	v_mfma_f32_32x32x16_bf16 v[2:17], v[54:57], v[38:41], v[2:17]
	v_mfma_f32_32x32x16_bf16 v[18:33], v[62:65], v[38:41], v[18:33]
	s_cmpk_eq_i32 s54, 0x180
	s_cselect_b32 s60, 0, 0x80
	s_cselect_b32 s56, 0, 0x100
	v_lshl_add_u64 v[100:101], v[100:101], 0, s[60:61]
	v_lshl_add_u64 v[102:103], v[102:103], 0, s[60:61]
	v_lshl_add_u64 v[104:105], v[104:105], 0, s[60:61]
	v_lshl_add_u64 v[106:107], v[106:107], 0, s[60:61]
	v_lshl_add_u64 v[46:47], v[46:47], 0, s[56:57]
	global_load_dwordx4 v[34:37], v[46:47], off offset:-112
	global_load_dwordx4 v[38:41], v[46:47], off offset:-128
	global_load_dwordx4 v[54:57], v[100:101], off
	global_load_dwordx4 v[62:65], v[104:105], off
	global_load_dwordx4 v[58:61], v[102:103], off
	global_load_dwordx4 v[66:69], v[106:107], off
	s_waitcnt vmcnt(11)
	v_cvt_pk_bf16_f32 v72, v76, v77
	s_waitcnt vmcnt(10)
	v_cvt_pk_bf16_f32 v70, v80, v81
	v_cvt_pk_bf16_f32 v71, v82, v83
	v_cvt_pk_bf16_f32 v73, v78, v79
	v_lshlrev_b32_e32 v74, 16, v70
	v_and_b32_e32 v75, 0xffff0000, v70
	s_waitcnt vmcnt(9)
	v_mfma_f32_32x32x16_bf16 v[2:17], v[84:87], v[70:73], v[2:17]
	v_add_f32_e64 v80, v80, -v74
	v_add_f32_e64 v81, v81, -v75
	v_lshlrev_b32_e32 v74, 16, v71
	v_and_b32_e32 v75, 0xffff0000, v71
	v_add_f32_e64 v82, v82, -v74
	v_add_f32_e64 v83, v83, -v75
	v_cvt_pk_bf16_f32 v80, v80, v81
	v_cvt_pk_bf16_f32 v81, v82, v83
	v_lshlrev_b32_e32 v82, 16, v72
	s_waitcnt vmcnt(8)
	v_mfma_f32_32x32x16_bf16 v[18:33], v[92:95], v[70:73], v[18:33]
	v_and_b32_e32 v83, 0xffff0000, v72
	v_add_f32_e64 v76, v76, -v82
	v_add_f32_e64 v77, v77, -v83
	v_cvt_pk_bf16_f32 v82, v76, v77
	v_lshlrev_b32_e32 v76, 16, v73
	v_and_b32_e32 v77, 0xffff0000, v73
	v_pk_add_f32 v[76:77], v[78:79], v[76:77] neg_lo:[0,1] neg_hi:[0,1]
	s_waitcnt vmcnt(7)
	v_mfma_f32_32x32x16_bf16 v[2:17], v[88:91], v[70:73], v[2:17]
	v_cvt_pk_bf16_f32 v83, v76, v77
	s_waitcnt vmcnt(6)
	v_mfma_f32_32x32x16_bf16 v[18:33], v[96:99], v[70:73], v[18:33]
	v_mfma_f32_32x32x16_bf16 v[2:17], v[84:87], v[80:83], v[2:17]
	v_mfma_f32_32x32x16_bf16 v[18:33], v[92:95], v[80:83], v[18:33]
	s_add_u32 s54, s54, 0x80
	s_addc_u32 s55, s55, 0
	s_cmpk_eq_i32 s54, 0x200
	s_cbranch_scc0 .LBB0_825
	s_waitcnt vmcnt(0)
	s_mov_b64 s[56:57], 0x100
	v_add_u32_e32 v34, 0x400, v160
	s_nop 8
	ds_write2_b32 v34, v2, v3 offset1:1
	v_add_u32_e32 v2, 0x480, v160
	ds_write2_b32 v2, v18, v19 offset1:1
	v_add_u32_e32 v2, 0x408, v160
	ds_write2_b32 v2, v4, v5 offset1:1
	v_add_u32_e32 v2, 0x488, v160
	ds_write2_b32 v2, v20, v21 offset1:1
	v_add_u32_e32 v2, 0x420, v160
	ds_write2_b32 v2, v6, v7 offset1:1
	v_add_u32_e32 v2, 0x4a0, v160
	ds_write2_b32 v2, v22, v23 offset1:1
	v_add_u32_e32 v2, 0x428, v160
	ds_write2_b32 v2, v8, v9 offset1:1
	v_add_u32_e32 v2, 0x4a8, v160
	ds_write2_b32 v2, v24, v25 offset1:1
	v_add_u32_e32 v2, 0x440, v160
	ds_write2_b32 v2, v10, v11 offset1:1
	v_add_u32_e32 v2, 0x4c0, v160
	ds_write2_b32 v2, v26, v27 offset1:1
	v_add_u32_e32 v2, 0x448, v160
	ds_write2_b32 v2, v12, v13 offset1:1
	v_add_u32_e32 v2, 0x4c8, v160
	s_lshl_b32 s56, s2, 5
	ds_write2_b32 v2, v28, v29 offset1:1
	v_add_u32_e32 v2, 0x460, v160
	v_readlane_b32 s54, v243, 36
	ds_write2_b32 v2, v14, v15 offset1:1
	v_add_u32_e32 v2, 0x4e0, v160
	s_add_i32 s62, s56, s54
	ds_write2_b32 v2, v30, v31 offset1:1
	v_add_u32_e32 v2, 0x468, v160
	s_ashr_i32 s63, s62, 31
	ds_write2_b32 v2, v16, v17 offset1:1
	v_add_u32_e32 v2, 0x4e8, v160
	s_lshl_b64 s[54:55], s[62:63], 13
	ds_write2_b32 v2, v32, v33 offset1:1
	v_lshl_add_u64 v[2:3], v[136:137], 0, s[54:55]
	s_waitcnt lgkmcnt(0)
	s_barrier
	global_load_dwordx4 v[126:129], v[2:3], off
	global_load_dwordx4 v[122:125], v[2:3], off offset:1024
	global_load_dwordx4 v[118:121], v[2:3], off offset:2048
	global_load_dwordx4 v[114:117], v[2:3], off offset:3072
	s_movk_i32 s57, 0x1000
	v_add_co_u32_e32 v2, vcc, s57, v2
	s_or_b32 s54, s62, 1
	s_nop 0
	v_addc_co_u32_e32 v3, vcc, 0, v3, vcc
	global_load_dwordx4 v[110:113], v[2:3], off
	global_load_dwordx4 v[106:109], v[2:3], off offset:1024
	global_load_dwordx4 v[102:105], v[2:3], off offset:2048
	global_load_dwordx4 v[98:101], v[2:3], off offset:3072
	s_ashr_i32 s55, s54, 31
	s_lshl_b64 s[54:55], s[54:55], 13
	v_lshl_add_u64 v[2:3], v[136:137], 0, s[54:55]
	s_or_b32 s54, s62, 2
	global_load_dwordx4 v[94:97], v[2:3], off
	global_load_dwordx4 v[90:93], v[2:3], off offset:1024
	global_load_dwordx4 v[86:89], v[2:3], off offset:2048
	global_load_dwordx4 v[82:85], v[2:3], off offset:3072
	v_add_co_u32_e32 v2, vcc, s57, v2
	s_ashr_i32 s55, s54, 31
	s_nop 0
	v_addc_co_u32_e32 v3, vcc, 0, v3, vcc
	s_lshl_b64 s[54:55], s[54:55], 13
	global_load_dwordx4 v[78:81], v[2:3], off
	global_load_dwordx4 v[74:77], v[2:3], off offset:1024
	global_load_dwordx4 v[70:73], v[2:3], off offset:2048
	global_load_dwordx4 v[66:69], v[2:3], off offset:3072
	v_lshl_add_u64 v[2:3], v[136:137], 0, s[54:55]
	s_or_b32 s54, s62, 3
	global_load_dwordx4 v[62:65], v[2:3], off
	global_load_dwordx4 v[58:61], v[2:3], off offset:1024
	global_load_dwordx4 v[54:57], v[2:3], off offset:2048
	global_load_dwordx4 v[50:53], v[2:3], off offset:3072
	v_add_co_u32_e32 v2, vcc, s57, v2
	s_ashr_i32 s55, s54, 31
	s_nop 0
	v_addc_co_u32_e32 v3, vcc, 0, v3, vcc
	s_lshl_b64 s[54:55], s[54:55], 13
	global_load_dwordx4 v[46:49], v[2:3], off
	global_load_dwordx4 v[42:45], v[2:3], off offset:1024
	global_load_dwordx4 v[38:41], v[2:3], off offset:2048
	global_load_dwordx4 v[34:37], v[2:3], off offset:3072
	v_lshl_add_u64 v[2:3], v[136:137], 0, s[54:55]
	global_load_dwordx4 v[30:33], v[2:3], off
	global_load_dwordx4 v[26:29], v[2:3], off offset:1024
	global_load_dwordx4 v[22:25], v[2:3], off offset:2048
	global_load_dwordx4 v[18:21], v[2:3], off offset:3072
	v_add_co_u32_e32 v2, vcc, s57, v2
	s_mov_b32 s54, 0xf800000
	s_nop 0
	v_addc_co_u32_e32 v3, vcc, 0, v3, vcc
	global_load_dwordx4 v[14:17], v[2:3], off
	global_load_dwordx4 v[10:13], v[2:3], off offset:1024
	global_load_dwordx4 v[6:9], v[2:3], off offset:2048
	s_nop 0
	global_load_dwordx4 v[2:5], v[2:3], off offset:3072
	s_waitcnt vmcnt(31)
	v_mul_f32_e32 v132, v127, v127
	v_mul_f32_e32 v151, v129, v129
	v_fmac_f32_e32 v132, v126, v126
	v_fmac_f32_e32 v151, v128, v128
	v_add_f32_e32 v132, v132, v151
	s_waitcnt vmcnt(30)
	v_mul_f32_e32 v151, v123, v123
	v_mul_f32_e32 v152, v125, v125
	v_fmac_f32_e32 v151, v122, v122
	v_fmac_f32_e32 v152, v124, v124
	v_add_f32_e32 v151, v151, v152
	v_add_f32_e32 v132, v132, v151
	s_waitcnt vmcnt(29)
	v_mul_f32_e32 v151, v119, v119
	v_mul_f32_e32 v152, v121, v121
	v_fmac_f32_e32 v151, v118, v118
	v_fmac_f32_e32 v152, v120, v120
	v_add_f32_e32 v151, v151, v152
	v_add_f32_e32 v132, v132, v151
	s_waitcnt vmcnt(28)
	v_mul_f32_e32 v151, v115, v115
	v_mul_f32_e32 v152, v117, v117
	v_fmac_f32_e32 v151, v114, v114
	v_fmac_f32_e32 v152, v116, v116
	v_add_f32_e32 v151, v151, v152
	v_add_f32_e32 v132, v132, v151
	s_waitcnt vmcnt(27)
	v_mul_f32_e32 v151, v111, v111
	v_mul_f32_e32 v152, v113, v113
	v_fmac_f32_e32 v151, v110, v110
	v_fmac_f32_e32 v152, v112, v112
	v_add_f32_e32 v151, v151, v152
	v_add_f32_e32 v132, v132, v151
	s_waitcnt vmcnt(26)
	v_mul_f32_e32 v151, v107, v107
	v_mul_f32_e32 v152, v109, v109
	v_fmac_f32_e32 v151, v106, v106
	v_fmac_f32_e32 v152, v108, v108
	v_add_f32_e32 v151, v151, v152
	v_add_f32_e32 v132, v132, v151
	s_waitcnt vmcnt(25)
	v_mul_f32_e32 v151, v103, v103
	v_mul_f32_e32 v152, v105, v105
	v_fmac_f32_e32 v151, v102, v102
	v_fmac_f32_e32 v152, v104, v104
	v_add_f32_e32 v151, v151, v152
	v_add_f32_e32 v132, v132, v151
	s_waitcnt vmcnt(24)
	v_mul_f32_e32 v151, v99, v99
	v_mul_f32_e32 v152, v101, v101
	v_fmac_f32_e32 v151, v98, v98
	v_fmac_f32_e32 v152, v100, v100
	v_add_f32_e32 v151, v151, v152
	v_add_f32_e32 v132, v132, v151
	ds_swizzle_b32 v151, v132 offset:swizzle(SWAP,1)
	s_waitcnt lgkmcnt(0)
	v_add_f32_e32 v132, v132, v151
	ds_swizzle_b32 v151, v132 offset:swizzle(SWAP,2)
	s_waitcnt lgkmcnt(0)
	v_add_f32_e32 v132, v132, v151
	ds_swizzle_b32 v151, v132 offset:swizzle(SWAP,4)
	s_waitcnt lgkmcnt(0)
	v_add_f32_e32 v132, v132, v151
	ds_swizzle_b32 v151, v132 offset:swizzle(SWAP,8)
	s_waitcnt lgkmcnt(0)
	v_add_f32_e32 v132, v132, v151
	ds_swizzle_b32 v151, v132 offset:swizzle(SWAP,16)
	s_waitcnt lgkmcnt(0)
	v_add_f32_e32 v132, v132, v151
	v_mov_b32_e32 v151, v132
	s_nop 1
	v_permlane32_swap_b32_e32 v132, v151
	v_add_f32_e32 v132, v132, v151
	v_fmamk_f32 v132, v132, 0x3a000000, v177
	v_mul_f32_e32 v151, 0x4f800000, v132
	v_cmp_gt_f32_e64 s[54:55], s54, v132
	s_nop 1
	v_cndmask_b32_e64 v132, v132, v151, s[54:55]
	v_sqrt_f32_e32 v151, v132
	s_nop 0
	v_add_u32_e32 v152, -1, v151
	v_fma_f32 v153, -v152, v151, v132
	v_cmp_ge_f32_e32 vcc, 0, v153
	v_add_u32_e32 v153, 1, v151
	s_nop 0
	v_cndmask_b32_e32 v152, v151, v152, vcc
	v_fma_f32 v151, -v153, v151, v132
	v_cmp_lt_f32_e32 vcc, 0, v151
	s_nop 1
	v_cndmask_b32_e32 v151, v152, v153, vcc
	v_mul_f32_e32 v152, 0x37800000, v151
	v_cndmask_b32_e64 v151, v151, v152, s[54:55]
	v_cmp_class_f32_e32 vcc, v132, v178
	s_nop 1
	v_cndmask_b32_e32 v132, v151, v132, vcc
	v_div_scale_f32 v151, s[54:55], v132, v132, 1.0
	v_rcp_f32_e32 v152, v151
	s_nop 0
	v_fma_f32 v153, -v151, v152, 1.0
	v_fmac_f32_e32 v152, v153, v152
	v_div_scale_f32 v153, vcc, 1.0, v132, 1.0
	v_mul_f32_e32 v182, v153, v152
	v_fma_f32 v183, -v151, v182, v153
	v_fmac_f32_e32 v182, v183, v152
	v_fma_f32 v151, -v151, v182, v153
	v_div_fmas_f32 v151, v151, v152, v182
	v_div_fixup_f32 v132, v151, v132, 1.0
	s_mov_b64 s[54:55], exec
	v_readlane_b32 s58, v243, 16
	v_readlane_b32 s59, v243, 17
	s_and_b64 s[58:59], s[54:55], s[58:59]
	s_mov_b64 exec, s[58:59]
	v_mov_b32_e32 v151, s64
	ds_write_b32 v151, v132
	s_or_b64 exec, exec, s[54:55]
	v_pk_mul_f32 v[186:187], v[132:133], v[128:129] op_sel_hi:[0,1]
	v_pk_mul_f32 v[188:189], v[132:133], v[126:127] op_sel_hi:[0,1]
	ds_read_b128 v[126:129], v161
	ds_read_b128 v[182:185], v162
	v_mov_b32_e32 v151, 0
	s_lshl_b64 s[54:55], s[62:63], 11
	v_lshl_add_u64 v[152:153], v[138:139], 0, s[54:55]
	s_mov_b32 s54, 0xf800000
	s_waitcnt lgkmcnt(0)
	v_pk_fma_f32 v[126:127], v[188:189], v[126:127], v[182:183]
	v_pk_fma_f32 v[128:129], v[186:187], v[128:129], v[184:185]
	v_cvt_pk_fp8_f32 v151, v126, v127
	v_pk_mul_f32 v[182:183], v[132:133], v[124:125] op_sel_hi:[0,1]
	v_pk_mul_f32 v[184:185], v[132:133], v[122:123] op_sel_hi:[0,1]
	v_cvt_pk_fp8_f32 v151, v128, v129 op_sel:[0,0,1]
	global_store_dword v[152:153], v151, off
	ds_read_b128 v[122:125], v163
	ds_read_b128 v[126:129], v164
	s_waitcnt lgkmcnt(0)
	v_pk_fma_f32 v[122:123], v[184:185], v[122:123], v[126:127]
	v_mov_b32_e32 v126, 0
	v_cvt_pk_fp8_f32 v126, v122, v123
	v_pk_fma_f32 v[124:125], v[182:183], v[124:125], v[128:129]
	v_pk_mul_f32 v[128:129], v[132:133], v[118:119] op_sel_hi:[0,1]
	v_cvt_pk_fp8_f32 v126, v124, v125 op_sel:[0,0,1]
	global_store_dword v[152:153], v126, off offset:256
	v_pk_mul_f32 v[126:127], v[132:133], v[120:121] op_sel_hi:[0,1]
	ds_read_b128 v[118:121], v165
	ds_read_b128 v[122:125], v166
	s_waitcnt lgkmcnt(0)
	v_pk_fma_f32 v[118:119], v[128:129], v[118:119], v[122:123]
	v_mov_b32_e32 v122, 0
	v_cvt_pk_fp8_f32 v122, v118, v119
	v_pk_fma_f32 v[120:121], v[126:127], v[120:121], v[124:125]
	v_pk_mul_f32 v[124:125], v[132:133], v[114:115] op_sel_hi:[0,1]
	v_cvt_pk_fp8_f32 v122, v120, v121 op_sel:[0,0,1]
	global_store_dword v[152:153], v122, off offset:512
	v_pk_mul_f32 v[122:123], v[132:133], v[116:117] op_sel_hi:[0,1]
	ds_read_b128 v[114:117], v167
	ds_read_b128 v[118:121], v168
	s_waitcnt lgkmcnt(0)
	v_pk_fma_f32 v[114:115], v[124:125], v[114:115], v[118:119]
	v_mov_b32_e32 v118, 0
	v_cvt_pk_fp8_f32 v118, v114, v115
	v_pk_fma_f32 v[116:117], v[122:123], v[116:117], v[120:121]
	v_pk_mul_f32 v[120:121], v[132:133], v[110:111] op_sel_hi:[0,1]
	v_cvt_pk_fp8_f32 v118, v116, v117 op_sel:[0,0,1]
	global_store_dword v[152:153], v118, off offset:768
	v_pk_mul_f32 v[118:119], v[132:133], v[112:113] op_sel_hi:[0,1]
	ds_read_b128 v[110:113], v169
	ds_read_b128 v[114:117], v170
	s_waitcnt lgkmcnt(0)
	v_pk_fma_f32 v[110:111], v[120:121], v[110:111], v[114:115]
	v_mov_b32_e32 v114, 0
	v_cvt_pk_fp8_f32 v114, v110, v111
	v_pk_fma_f32 v[112:113], v[118:119], v[112:113], v[116:117]
	v_pk_mul_f32 v[116:117], v[132:133], v[106:107] op_sel_hi:[0,1]
	v_cvt_pk_fp8_f32 v114, v112, v113 op_sel:[0,0,1]
	global_store_dword v[152:153], v114, off offset:1024
	v_pk_mul_f32 v[114:115], v[132:133], v[108:109] op_sel_hi:[0,1]
	ds_read_b128 v[106:109], v171
	ds_read_b128 v[110:113], v172
	s_waitcnt lgkmcnt(0)
	v_pk_fma_f32 v[106:107], v[116:117], v[106:107], v[110:111]
	v_mov_b32_e32 v110, 0
	v_cvt_pk_fp8_f32 v110, v106, v107
	v_pk_fma_f32 v[108:109], v[114:115], v[108:109], v[112:113]
	v_pk_mul_f32 v[112:113], v[132:133], v[102:103] op_sel_hi:[0,1]
	v_cvt_pk_fp8_f32 v110, v108, v109 op_sel:[0,0,1]
	global_store_dword v[152:153], v110, off offset:1280
	v_pk_mul_f32 v[110:111], v[132:133], v[104:105] op_sel_hi:[0,1]
	ds_read_b128 v[102:105], v173
	ds_read_b128 v[106:109], v174
	s_waitcnt lgkmcnt(0)
	v_pk_fma_f32 v[102:103], v[112:113], v[102:103], v[106:107]
	v_mov_b32_e32 v106, 0
	v_cvt_pk_fp8_f32 v106, v102, v103
	v_pk_fma_f32 v[104:105], v[110:111], v[104:105], v[108:109]
	v_pk_mul_f32 v[108:109], v[132:133], v[98:99] op_sel_hi:[0,1]
	v_cvt_pk_fp8_f32 v106, v104, v105 op_sel:[0,0,1]
	global_store_dword v[152:153], v106, off offset:1536
	v_pk_mul_f32 v[106:107], v[132:133], v[100:101] op_sel_hi:[0,1]
	ds_read_b128 v[98:101], v175
	ds_read_b128 v[102:105], v176
	s_waitcnt lgkmcnt(0)
	v_pk_fma_f32 v[98:99], v[108:109], v[98:99], v[102:103]
	v_mov_b32_e32 v102, 0
	v_cvt_pk_fp8_f32 v102, v98, v99
	s_waitcnt vmcnt(30)
	v_mul_f32_e32 v98, v95, v95
	v_mul_f32_e32 v99, v97, v97
	v_pk_fma_f32 v[100:101], v[106:107], v[100:101], v[104:105]
	v_fmac_f32_e32 v98, v94, v94
	v_fmac_f32_e32 v99, v96, v96
	v_cvt_pk_fp8_f32 v102, v100, v101 op_sel:[0,0,1]
	v_add_f32_e32 v98, v98, v99
	s_waitcnt vmcnt(29)
	v_mul_f32_e32 v99, v91, v91
	v_mul_f32_e32 v100, v93, v93
	v_fmac_f32_e32 v99, v90, v90
	v_fmac_f32_e32 v100, v92, v92
	v_add_f32_e32 v99, v99, v100
	v_add_f32_e32 v98, v98, v99
	s_waitcnt vmcnt(28)
	v_mul_f32_e32 v99, v87, v87
	v_mul_f32_e32 v100, v89, v89
	v_fmac_f32_e32 v99, v86, v86
	v_fmac_f32_e32 v100, v88, v88
	v_add_f32_e32 v99, v99, v100
	v_add_f32_e32 v98, v98, v99
	s_waitcnt vmcnt(27)
	v_mul_f32_e32 v99, v83, v83
	v_mul_f32_e32 v100, v85, v85
	v_fmac_f32_e32 v99, v82, v82
	v_fmac_f32_e32 v100, v84, v84
	v_add_f32_e32 v99, v99, v100
	v_add_f32_e32 v98, v98, v99
	s_waitcnt vmcnt(26)
	v_mul_f32_e32 v99, v79, v79
	v_mul_f32_e32 v100, v81, v81
	v_fmac_f32_e32 v99, v78, v78
	v_fmac_f32_e32 v100, v80, v80
	v_add_f32_e32 v99, v99, v100
	v_add_f32_e32 v98, v98, v99
	s_waitcnt vmcnt(25)
	v_mul_f32_e32 v99, v75, v75
	v_mul_f32_e32 v100, v77, v77
	v_fmac_f32_e32 v99, v74, v74
	v_fmac_f32_e32 v100, v76, v76
	v_add_f32_e32 v99, v99, v100
	v_add_f32_e32 v98, v98, v99
	s_waitcnt vmcnt(24)
	v_mul_f32_e32 v99, v71, v71
	v_mul_f32_e32 v100, v73, v73
	v_fmac_f32_e32 v99, v70, v70
	v_fmac_f32_e32 v100, v72, v72
	v_add_f32_e32 v99, v99, v100
	v_add_f32_e32 v98, v98, v99
	s_waitcnt vmcnt(23)
	v_mul_f32_e32 v99, v67, v67
	v_mul_f32_e32 v100, v69, v69
	v_fmac_f32_e32 v99, v66, v66
	v_fmac_f32_e32 v100, v68, v68
	v_add_f32_e32 v99, v99, v100
	v_add_f32_e32 v98, v98, v99
	ds_swizzle_b32 v99, v98 offset:swizzle(SWAP,1)
	global_store_dword v[152:153], v102, off offset:1792
	s_waitcnt lgkmcnt(0)
	v_add_f32_e32 v98, v98, v99
	ds_swizzle_b32 v99, v98 offset:swizzle(SWAP,2)
	s_waitcnt lgkmcnt(0)
	v_add_f32_e32 v98, v98, v99
	ds_swizzle_b32 v99, v98 offset:swizzle(SWAP,4)
	s_waitcnt lgkmcnt(0)
	v_add_f32_e32 v98, v98, v99
	ds_swizzle_b32 v99, v98 offset:swizzle(SWAP,8)
	s_waitcnt lgkmcnt(0)
	v_add_f32_e32 v98, v98, v99
	ds_swizzle_b32 v99, v98 offset:swizzle(SWAP,16)
	s_waitcnt lgkmcnt(0)
	v_add_f32_e32 v98, v98, v99
	v_mov_b32_e32 v99, v98
	s_nop 1
	v_permlane32_swap_b32_e32 v98, v99
	v_add_f32_e32 v98, v98, v99
	v_fmamk_f32 v98, v98, 0x3a000000, v177
	v_cmp_gt_f32_e32 vcc, s54, v98
	v_mul_f32_e32 v99, 0x4f800000, v98
	s_nop 0
	v_cndmask_b32_e32 v98, v98, v99, vcc
	v_sqrt_f32_e32 v99, v98
	s_nop 0
	v_add_u32_e32 v100, -1, v99
	v_fma_f32 v101, -v100, v99, v98
	v_cmp_ge_f32_e64 s[54:55], 0, v101
	v_add_u32_e32 v101, 1, v99
	s_nop 0
	v_cndmask_b32_e64 v100, v99, v100, s[54:55]
	v_fma_f32 v99, -v101, v99, v98
	v_cmp_lt_f32_e64 s[54:55], 0, v99
	s_nop 1
	v_cndmask_b32_e64 v99, v100, v101, s[54:55]
	v_mul_f32_e32 v100, 0x37800000, v99
	v_cndmask_b32_e32 v99, v99, v100, vcc
	v_cmp_class_f32_e32 vcc, v98, v178
	s_nop 1
	v_cndmask_b32_e32 v98, v99, v98, vcc
	v_div_scale_f32 v99, s[54:55], v98, v98, 1.0
	v_rcp_f32_e32 v100, v99
	s_nop 0
	v_fma_f32 v101, -v99, v100, 1.0
	v_fmac_f32_e32 v100, v101, v100
	v_div_scale_f32 v101, vcc, 1.0, v98, 1.0
	v_mul_f32_e32 v102, v101, v100
	v_fma_f32 v103, -v99, v102, v101
	v_fmac_f32_e32 v102, v103, v100
	v_fma_f32 v99, -v99, v102, v101
	v_div_fmas_f32 v99, v99, v100, v102
	v_div_fixup_f32 v98, v99, v98, 1.0
	s_mov_b64 s[54:55], exec
	v_readlane_b32 s58, v243, 16
	v_readlane_b32 s59, v243, 17
	s_and_b64 s[58:59], s[54:55], s[58:59]
	s_mov_b64 exec, s[58:59]
	v_mov_b32_e32 v99, s64
	ds_write_b32 v99, v98 offset:4
	s_or_b64 exec, exec, s[54:55]
	v_pk_mul_f32 v[106:107], v[98:99], v[96:97] op_sel_hi:[0,1]
	v_pk_mul_f32 v[108:109], v[98:99], v[94:95] op_sel_hi:[0,1]
	ds_read_b128 v[94:97], v161
	ds_read_b128 v[102:105], v162
	v_mov_b32_e32 v99, 0
	v_readlane_b32 s54, v243, 34
	s_add_i32 s60, s54, s56
	s_ashr_i32 s61, s60, 31
	s_waitcnt lgkmcnt(0)
	v_pk_fma_f32 v[94:95], v[108:109], v[94:95], v[102:103]
	v_pk_fma_f32 v[96:97], v[106:107], v[96:97], v[104:105]
	v_cvt_pk_fp8_f32 v99, v94, v95
	s_lshl_b64 s[54:55], s[60:61], 11
	v_lshl_add_u64 v[100:101], v[138:139], 0, s[54:55]
	s_mov_b32 s54, 0xf800000
	v_cvt_pk_fp8_f32 v99, v96, v97 op_sel:[0,0,1]
	global_store_dword v[100:101], v99, off
	v_pk_mul_f32 v[102:103], v[98:99], v[92:93] op_sel_hi:[0,1]
	v_pk_mul_f32 v[104:105], v[98:99], v[90:91] op_sel_hi:[0,1]
	ds_read_b128 v[90:93], v163
	ds_read_b128 v[94:97], v164
	s_waitcnt lgkmcnt(0)
	v_pk_fma_f32 v[90:91], v[104:105], v[90:91], v[94:95]
	v_mov_b32_e32 v94, 0
	v_cvt_pk_fp8_f32 v94, v90, v91
	v_pk_fma_f32 v[92:93], v[102:103], v[92:93], v[96:97]
	v_pk_mul_f32 v[96:97], v[98:99], v[86:87] op_sel_hi:[0,1]
	v_cvt_pk_fp8_f32 v94, v92, v93 op_sel:[0,0,1]
	global_store_dword v[100:101], v94, off offset:256
	v_pk_mul_f32 v[94:95], v[98:99], v[88:89] op_sel_hi:[0,1]
	ds_read_b128 v[86:89], v165
	ds_read_b128 v[90:93], v166
	s_waitcnt lgkmcnt(0)
	v_pk_fma_f32 v[86:87], v[96:97], v[86:87], v[90:91]
	v_mov_b32_e32 v90, 0
	v_cvt_pk_fp8_f32 v90, v86, v87
	v_pk_fma_f32 v[88:89], v[94:95], v[88:89], v[92:93]
	v_pk_mul_f32 v[92:93], v[98:99], v[82:83] op_sel_hi:[0,1]
	v_cvt_pk_fp8_f32 v90, v88, v89 op_sel:[0,0,1]
	global_store_dword v[100:101], v90, off offset:512
	v_pk_mul_f32 v[90:91], v[98:99], v[84:85] op_sel_hi:[0,1]
	ds_read_b128 v[82:85], v167
	ds_read_b128 v[86:89], v168
	s_waitcnt lgkmcnt(0)
	v_pk_fma_f32 v[82:83], v[92:93], v[82:83], v[86:87]
	v_mov_b32_e32 v86, 0
	v_cvt_pk_fp8_f32 v86, v82, v83
	v_pk_fma_f32 v[84:85], v[90:91], v[84:85], v[88:89]
	v_pk_mul_f32 v[88:89], v[98:99], v[78:79] op_sel_hi:[0,1]
	v_cvt_pk_fp8_f32 v86, v84, v85 op_sel:[0,0,1]
	global_store_dword v[100:101], v86, off offset:768
	v_pk_mul_f32 v[86:87], v[98:99], v[80:81] op_sel_hi:[0,1]
	ds_read_b128 v[78:81], v169
	ds_read_b128 v[82:85], v170
	s_waitcnt lgkmcnt(0)
	v_pk_fma_f32 v[78:79], v[88:89], v[78:79], v[82:83]
	v_mov_b32_e32 v82, 0
	v_cvt_pk_fp8_f32 v82, v78, v79
	v_pk_fma_f32 v[80:81], v[86:87], v[80:81], v[84:85]
	v_pk_mul_f32 v[84:85], v[98:99], v[74:75] op_sel_hi:[0,1]
	v_cvt_pk_fp8_f32 v82, v80, v81 op_sel:[0,0,1]
	global_store_dword v[100:101], v82, off offset:1024
	v_pk_mul_f32 v[82:83], v[98:99], v[76:77] op_sel_hi:[0,1]
	ds_read_b128 v[74:77], v171
	ds_read_b128 v[78:81], v172
	s_waitcnt lgkmcnt(0)
	v_pk_fma_f32 v[74:75], v[84:85], v[74:75], v[78:79]
	v_mov_b32_e32 v78, 0
	v_cvt_pk_fp8_f32 v78, v74, v75
	v_pk_fma_f32 v[76:77], v[82:83], v[76:77], v[80:81]
	v_pk_mul_f32 v[80:81], v[98:99], v[70:71] op_sel_hi:[0,1]
	v_cvt_pk_fp8_f32 v78, v76, v77 op_sel:[0,0,1]
	global_store_dword v[100:101], v78, off offset:1280
	v_pk_mul_f32 v[78:79], v[98:99], v[72:73] op_sel_hi:[0,1]
	ds_read_b128 v[70:73], v173
	ds_read_b128 v[74:77], v174
	s_waitcnt lgkmcnt(0)
	v_pk_fma_f32 v[70:71], v[80:81], v[70:71], v[74:75]
	v_mov_b32_e32 v74, 0
	v_cvt_pk_fp8_f32 v74, v70, v71
	v_pk_fma_f32 v[72:73], v[78:79], v[72:73], v[76:77]
	v_pk_mul_f32 v[76:77], v[98:99], v[66:67] op_sel_hi:[0,1]
	v_cvt_pk_fp8_f32 v74, v72, v73 op_sel:[0,0,1]
	global_store_dword v[100:101], v74, off offset:1536
	v_pk_mul_f32 v[74:75], v[98:99], v[68:69] op_sel_hi:[0,1]
	ds_read_b128 v[66:69], v175
	ds_read_b128 v[70:73], v176
	s_waitcnt lgkmcnt(0)
	v_pk_fma_f32 v[66:67], v[76:77], v[66:67], v[70:71]
	v_mov_b32_e32 v70, 0
	v_cvt_pk_fp8_f32 v70, v66, v67
	s_waitcnt vmcnt(30)
	v_mul_f32_e32 v66, v63, v63
	v_mul_f32_e32 v67, v65, v65
	v_pk_fma_f32 v[68:69], v[74:75], v[68:69], v[72:73]
	v_fmac_f32_e32 v66, v62, v62
	v_fmac_f32_e32 v67, v64, v64
	v_cvt_pk_fp8_f32 v70, v68, v69 op_sel:[0,0,1]
	v_add_f32_e32 v66, v66, v67
	s_waitcnt vmcnt(29)
	v_mul_f32_e32 v67, v59, v59
	v_mul_f32_e32 v68, v61, v61
	v_fmac_f32_e32 v67, v58, v58
	v_fmac_f32_e32 v68, v60, v60
	v_add_f32_e32 v67, v67, v68
	v_add_f32_e32 v66, v66, v67
	s_waitcnt vmcnt(28)
	v_mul_f32_e32 v67, v55, v55
	v_mul_f32_e32 v68, v57, v57
	v_fmac_f32_e32 v67, v54, v54
	v_fmac_f32_e32 v68, v56, v56
	v_add_f32_e32 v67, v67, v68
	v_add_f32_e32 v66, v66, v67
	s_waitcnt vmcnt(27)
	v_mul_f32_e32 v67, v51, v51
	v_mul_f32_e32 v68, v53, v53
	v_fmac_f32_e32 v67, v50, v50
	v_fmac_f32_e32 v68, v52, v52
	v_add_f32_e32 v67, v67, v68
	v_add_f32_e32 v66, v66, v67
	s_waitcnt vmcnt(26)
	v_mul_f32_e32 v67, v47, v47
	v_mul_f32_e32 v68, v49, v49
	v_fmac_f32_e32 v67, v46, v46
	v_fmac_f32_e32 v68, v48, v48
	v_add_f32_e32 v67, v67, v68
	v_add_f32_e32 v66, v66, v67
	s_waitcnt vmcnt(25)
	v_mul_f32_e32 v67, v43, v43
	v_mul_f32_e32 v68, v45, v45
	v_fmac_f32_e32 v67, v42, v42
	v_fmac_f32_e32 v68, v44, v44
	v_add_f32_e32 v67, v67, v68
	v_add_f32_e32 v66, v66, v67
	s_waitcnt vmcnt(24)
	v_mul_f32_e32 v67, v39, v39
	v_mul_f32_e32 v68, v41, v41
	v_fmac_f32_e32 v67, v38, v38
	v_fmac_f32_e32 v68, v40, v40
	v_add_f32_e32 v67, v67, v68
	v_add_f32_e32 v66, v66, v67
	s_waitcnt vmcnt(23)
	v_mul_f32_e32 v67, v35, v35
	v_mul_f32_e32 v68, v37, v37
	v_fmac_f32_e32 v67, v34, v34
	v_fmac_f32_e32 v68, v36, v36
	v_add_f32_e32 v67, v67, v68
	v_add_f32_e32 v66, v66, v67
	ds_swizzle_b32 v67, v66 offset:swizzle(SWAP,1)
	global_store_dword v[100:101], v70, off offset:1792
	s_waitcnt lgkmcnt(0)
	v_add_f32_e32 v66, v66, v67
	ds_swizzle_b32 v67, v66 offset:swizzle(SWAP,2)
	s_waitcnt lgkmcnt(0)
	v_add_f32_e32 v66, v66, v67
	ds_swizzle_b32 v67, v66 offset:swizzle(SWAP,4)
	s_waitcnt lgkmcnt(0)
	v_add_f32_e32 v66, v66, v67
	ds_swizzle_b32 v67, v66 offset:swizzle(SWAP,8)
	s_waitcnt lgkmcnt(0)
	v_add_f32_e32 v66, v66, v67
	ds_swizzle_b32 v67, v66 offset:swizzle(SWAP,16)
	s_waitcnt lgkmcnt(0)
	v_add_f32_e32 v66, v66, v67
	v_mov_b32_e32 v67, v66
	s_nop 1
	v_permlane32_swap_b32_e32 v66, v67
	v_add_f32_e32 v66, v66, v67
	v_fmamk_f32 v66, v66, 0x3a000000, v177
	v_cmp_gt_f32_e32 vcc, s54, v66
	v_mul_f32_e32 v67, 0x4f800000, v66
	s_nop 0
	v_cndmask_b32_e32 v66, v66, v67, vcc
	v_sqrt_f32_e32 v67, v66
	s_nop 0
	v_add_u32_e32 v68, -1, v67
	v_fma_f32 v69, -v68, v67, v66
	v_cmp_ge_f32_e64 s[54:55], 0, v69
	v_add_u32_e32 v69, 1, v67
	s_nop 0
	v_cndmask_b32_e64 v68, v67, v68, s[54:55]
	v_fma_f32 v67, -v69, v67, v66
	v_cmp_lt_f32_e64 s[54:55], 0, v67
	s_nop 1
	v_cndmask_b32_e64 v67, v68, v69, s[54:55]
	v_mul_f32_e32 v68, 0x37800000, v67
	v_cndmask_b32_e32 v67, v67, v68, vcc
	v_cmp_class_f32_e32 vcc, v66, v178
	s_nop 1
	v_cndmask_b32_e32 v66, v67, v66, vcc
	v_div_scale_f32 v67, s[54:55], v66, v66, 1.0
	v_rcp_f32_e32 v68, v67
	s_nop 0
	v_fma_f32 v69, -v67, v68, 1.0
	v_fmac_f32_e32 v68, v69, v68
	v_div_scale_f32 v69, vcc, 1.0, v66, 1.0
	v_mul_f32_e32 v70, v69, v68
	v_fma_f32 v71, -v67, v70, v69
	v_fmac_f32_e32 v70, v71, v68
	v_fma_f32 v67, -v67, v70, v69
	v_div_fmas_f32 v67, v67, v68, v70
	v_div_fixup_f32 v66, v67, v66, 1.0
	s_mov_b64 s[54:55], exec
	v_readlane_b32 s58, v243, 16
	v_readlane_b32 s59, v243, 17
	s_and_b64 s[58:59], s[54:55], s[58:59]
	s_mov_b64 exec, s[58:59]
	v_mov_b32_e32 v67, s64
	ds_write_b32 v67, v66 offset:8
	s_or_b64 exec, exec, s[54:55]
	v_pk_mul_f32 v[74:75], v[66:67], v[64:65] op_sel_hi:[0,1]
	v_pk_mul_f32 v[76:77], v[66:67], v[62:63] op_sel_hi:[0,1]
	ds_read_b128 v[62:65], v161
	ds_read_b128 v[70:73], v162
	v_mov_b32_e32 v67, 0
	v_readlane_b32 s54, v243, 35
	s_add_i32 s58, s54, s56
	s_ashr_i32 s59, s58, 31
	s_waitcnt lgkmcnt(0)
	v_pk_fma_f32 v[62:63], v[76:77], v[62:63], v[70:71]
	v_pk_fma_f32 v[64:65], v[74:75], v[64:65], v[72:73]
	v_cvt_pk_fp8_f32 v67, v62, v63
	s_lshl_b64 s[54:55], s[58:59], 11
	v_lshl_add_u64 v[68:69], v[138:139], 0, s[54:55]
	s_mov_b32 s54, 0xf800000
	v_cvt_pk_fp8_f32 v67, v64, v65 op_sel:[0,0,1]
	v_readlane_b32 s66, v243, 16
	v_readlane_b32 s67, v243, 17
	global_store_dword v[68:69], v67, off
	v_pk_mul_f32 v[70:71], v[66:67], v[60:61] op_sel_hi:[0,1]
	v_pk_mul_f32 v[72:73], v[66:67], v[58:59] op_sel_hi:[0,1]
	ds_read_b128 v[58:61], v163
	ds_read_b128 v[62:65], v164
	s_waitcnt lgkmcnt(0)
	v_pk_fma_f32 v[58:59], v[72:73], v[58:59], v[62:63]
	v_mov_b32_e32 v62, 0
	v_cvt_pk_fp8_f32 v62, v58, v59
	v_pk_fma_f32 v[60:61], v[70:71], v[60:61], v[64:65]
	v_pk_mul_f32 v[64:65], v[66:67], v[54:55] op_sel_hi:[0,1]
	v_cvt_pk_fp8_f32 v62, v60, v61 op_sel:[0,0,1]
	global_store_dword v[68:69], v62, off offset:256
	v_pk_mul_f32 v[62:63], v[66:67], v[56:57] op_sel_hi:[0,1]
	ds_read_b128 v[54:57], v165
	ds_read_b128 v[58:61], v166
	s_waitcnt lgkmcnt(0)
	v_pk_fma_f32 v[54:55], v[64:65], v[54:55], v[58:59]
	v_mov_b32_e32 v58, 0
	v_cvt_pk_fp8_f32 v58, v54, v55
	v_pk_fma_f32 v[56:57], v[62:63], v[56:57], v[60:61]
	v_pk_mul_f32 v[60:61], v[66:67], v[50:51] op_sel_hi:[0,1]
	v_cvt_pk_fp8_f32 v58, v56, v57 op_sel:[0,0,1]
	global_store_dword v[68:69], v58, off offset:512
	v_pk_mul_f32 v[58:59], v[66:67], v[52:53] op_sel_hi:[0,1]
	ds_read_b128 v[50:53], v167
	ds_read_b128 v[54:57], v168
	s_waitcnt lgkmcnt(0)
	v_pk_fma_f32 v[50:51], v[60:61], v[50:51], v[54:55]
	v_mov_b32_e32 v54, 0
	v_cvt_pk_fp8_f32 v54, v50, v51
	v_pk_fma_f32 v[52:53], v[58:59], v[52:53], v[56:57]
	v_pk_mul_f32 v[56:57], v[66:67], v[46:47] op_sel_hi:[0,1]
	v_cvt_pk_fp8_f32 v54, v52, v53 op_sel:[0,0,1]
	global_store_dword v[68:69], v54, off offset:768
	v_pk_mul_f32 v[54:55], v[66:67], v[48:49] op_sel_hi:[0,1]
	ds_read_b128 v[46:49], v169
	ds_read_b128 v[50:53], v170
	s_waitcnt lgkmcnt(0)
	v_pk_fma_f32 v[46:47], v[56:57], v[46:47], v[50:51]
	v_mov_b32_e32 v50, 0
	v_cvt_pk_fp8_f32 v50, v46, v47
	v_pk_fma_f32 v[48:49], v[54:55], v[48:49], v[52:53]
	v_pk_mul_f32 v[52:53], v[66:67], v[42:43] op_sel_hi:[0,1]
	v_cvt_pk_fp8_f32 v50, v48, v49 op_sel:[0,0,1]
	global_store_dword v[68:69], v50, off offset:1024
	v_pk_mul_f32 v[50:51], v[66:67], v[44:45] op_sel_hi:[0,1]
	ds_read_b128 v[42:45], v171
	ds_read_b128 v[46:49], v172
	s_waitcnt lgkmcnt(0)
	v_pk_fma_f32 v[42:43], v[52:53], v[42:43], v[46:47]
	v_mov_b32_e32 v46, 0
	v_cvt_pk_fp8_f32 v46, v42, v43
	v_pk_fma_f32 v[44:45], v[50:51], v[44:45], v[48:49]
	v_pk_mul_f32 v[48:49], v[66:67], v[38:39] op_sel_hi:[0,1]
	v_cvt_pk_fp8_f32 v46, v44, v45 op_sel:[0,0,1]
	global_store_dword v[68:69], v46, off offset:1280
	v_pk_mul_f32 v[46:47], v[66:67], v[40:41] op_sel_hi:[0,1]
	ds_read_b128 v[38:41], v173
	ds_read_b128 v[42:45], v174
	s_waitcnt lgkmcnt(0)
	v_pk_fma_f32 v[38:39], v[48:49], v[38:39], v[42:43]
	v_mov_b32_e32 v42, 0
	v_cvt_pk_fp8_f32 v42, v38, v39
	v_pk_fma_f32 v[40:41], v[46:47], v[40:41], v[44:45]
	v_pk_mul_f32 v[44:45], v[66:67], v[34:35] op_sel_hi:[0,1]
	v_cvt_pk_fp8_f32 v42, v40, v41 op_sel:[0,0,1]
	global_store_dword v[68:69], v42, off offset:1536
	v_pk_mul_f32 v[42:43], v[66:67], v[36:37] op_sel_hi:[0,1]
	ds_read_b128 v[34:37], v175
	ds_read_b128 v[38:41], v176
	s_waitcnt lgkmcnt(0)
	v_pk_fma_f32 v[34:35], v[44:45], v[34:35], v[38:39]
	v_mov_b32_e32 v38, 0
	v_cvt_pk_fp8_f32 v38, v34, v35
	s_waitcnt vmcnt(30)
	v_mul_f32_e32 v34, v31, v31
	v_mul_f32_e32 v35, v33, v33
	v_pk_fma_f32 v[36:37], v[42:43], v[36:37], v[40:41]
	v_fmac_f32_e32 v34, v30, v30
	v_fmac_f32_e32 v35, v32, v32
	v_cvt_pk_fp8_f32 v38, v36, v37 op_sel:[0,0,1]
	v_add_f32_e32 v34, v34, v35
	s_waitcnt vmcnt(29)
	v_mul_f32_e32 v35, v27, v27
	v_mul_f32_e32 v36, v29, v29
	v_fmac_f32_e32 v35, v26, v26
	v_fmac_f32_e32 v36, v28, v28
	v_add_f32_e32 v35, v35, v36
	v_add_f32_e32 v34, v34, v35
	s_waitcnt vmcnt(28)
	v_mul_f32_e32 v35, v23, v23
	v_mul_f32_e32 v36, v25, v25
	v_fmac_f32_e32 v35, v22, v22
	v_fmac_f32_e32 v36, v24, v24
	v_add_f32_e32 v35, v35, v36
	v_add_f32_e32 v34, v34, v35
	s_waitcnt vmcnt(27)
	v_mul_f32_e32 v35, v19, v19
	v_mul_f32_e32 v36, v21, v21
	v_fmac_f32_e32 v35, v18, v18
	v_fmac_f32_e32 v36, v20, v20
	v_add_f32_e32 v35, v35, v36
	v_add_f32_e32 v34, v34, v35
	s_waitcnt vmcnt(26)
	v_mul_f32_e32 v35, v15, v15
	v_mul_f32_e32 v36, v17, v17
	v_fmac_f32_e32 v35, v14, v14
	v_fmac_f32_e32 v36, v16, v16
	v_add_f32_e32 v35, v35, v36
	v_add_f32_e32 v34, v34, v35
	s_waitcnt vmcnt(25)
	v_mul_f32_e32 v35, v11, v11
	v_mul_f32_e32 v36, v13, v13
	v_fmac_f32_e32 v35, v10, v10
	v_fmac_f32_e32 v36, v12, v12
	v_add_f32_e32 v35, v35, v36
	v_add_f32_e32 v34, v34, v35
	s_waitcnt vmcnt(24)
	v_mul_f32_e32 v35, v7, v7
	v_mul_f32_e32 v36, v9, v9
	v_fmac_f32_e32 v35, v6, v6
	v_fmac_f32_e32 v36, v8, v8
	v_add_f32_e32 v35, v35, v36
	v_add_f32_e32 v34, v34, v35
	s_waitcnt vmcnt(23)
	v_mul_f32_e32 v35, v3, v3
	v_mul_f32_e32 v36, v5, v5
	v_fmac_f32_e32 v35, v2, v2
	v_fmac_f32_e32 v36, v4, v4
	v_add_f32_e32 v35, v35, v36
	v_add_f32_e32 v34, v34, v35
	ds_swizzle_b32 v35, v34 offset:swizzle(SWAP,1)
	global_store_dword v[68:69], v38, off offset:1792
	s_waitcnt lgkmcnt(0)
	v_add_f32_e32 v34, v34, v35
	ds_swizzle_b32 v35, v34 offset:swizzle(SWAP,2)
	s_waitcnt lgkmcnt(0)
	v_add_f32_e32 v34, v34, v35
	ds_swizzle_b32 v35, v34 offset:swizzle(SWAP,4)
	s_waitcnt lgkmcnt(0)
	v_add_f32_e32 v34, v34, v35
	ds_swizzle_b32 v35, v34 offset:swizzle(SWAP,8)
	s_waitcnt lgkmcnt(0)
	v_add_f32_e32 v34, v34, v35
	ds_swizzle_b32 v35, v34 offset:swizzle(SWAP,16)
	s_waitcnt lgkmcnt(0)
	v_add_f32_e32 v34, v34, v35
	v_mov_b32_e32 v35, v34
	s_nop 1
	v_permlane32_swap_b32_e32 v34, v35
	v_add_f32_e32 v34, v34, v35
	v_fmamk_f32 v34, v34, 0x3a000000, v177
	v_cmp_gt_f32_e32 vcc, s54, v34
	v_mul_f32_e32 v35, 0x4f800000, v34
	s_nop 0
	v_cndmask_b32_e32 v34, v34, v35, vcc
	v_sqrt_f32_e32 v35, v34
	s_nop 0
	v_add_u32_e32 v36, -1, v35
	v_fma_f32 v37, -v36, v35, v34
	v_cmp_ge_f32_e64 s[54:55], 0, v37
	v_add_u32_e32 v37, 1, v35
	s_nop 0
	v_cndmask_b32_e64 v36, v35, v36, s[54:55]
	v_fma_f32 v35, -v37, v35, v34
	v_cmp_lt_f32_e64 s[54:55], 0, v35
	s_nop 1
	v_cndmask_b32_e64 v35, v36, v37, s[54:55]
	v_mul_f32_e32 v36, 0x37800000, v35
	v_cndmask_b32_e32 v35, v35, v36, vcc
	v_cmp_class_f32_e32 vcc, v34, v178
	s_nop 1
	v_cndmask_b32_e32 v34, v35, v34, vcc
	v_div_scale_f32 v35, s[54:55], v34, v34, 1.0
	v_rcp_f32_e32 v36, v35
	s_nop 0
	v_fma_f32 v37, -v35, v36, 1.0
	v_fmac_f32_e32 v36, v37, v36
	v_div_scale_f32 v37, vcc, 1.0, v34, 1.0
	v_mul_f32_e32 v38, v37, v36
	v_fma_f32 v39, -v35, v38, v37
	v_fmac_f32_e32 v38, v39, v36
	v_fma_f32 v35, -v35, v38, v37
	v_div_fmas_f32 v35, v35, v36, v38
	v_div_fixup_f32 v34, v35, v34, 1.0
	s_and_saveexec_b64 s[54:55], s[66:67]
	v_mov_b32_e32 v35, s64
	ds_write_b32 v35, v34 offset:12
	s_or_b64 exec, exec, s[54:55]
	v_pk_mul_f32 v[42:43], v[34:35], v[32:33] op_sel_hi:[0,1]
	v_pk_mul_f32 v[44:45], v[34:35], v[30:31] op_sel_hi:[0,1]
	ds_read_b128 v[30:33], v161
	ds_read_b128 v[36:39], v162
	v_mov_b32_e32 v35, 0
	v_readlane_b32 s54, v243, 37
	s_add_i32 s56, s54, s56
	s_ashr_i32 s57, s56, 31
	s_waitcnt lgkmcnt(0)
	v_pk_fma_f32 v[30:31], v[44:45], v[30:31], v[36:37]
	v_pk_fma_f32 v[32:33], v[42:43], v[32:33], v[38:39]
	v_cvt_pk_fp8_f32 v35, v30, v31
	s_lshl_b64 s[54:55], s[56:57], 11
	v_lshl_add_u64 v[40:41], v[138:139], 0, s[54:55]
	v_readlane_b32 s54, v243, 32
	v_cvt_pk_fp8_f32 v35, v32, v33 op_sel:[0,0,1]
	v_readlane_b32 s55, v243, 33
	v_readlane_b32 s66, v243, 38
	v_readlane_b32 s67, v243, 39
	global_store_dword v[40:41], v35, off
	v_pk_mul_f32 v[36:37], v[34:35], v[28:29] op_sel_hi:[0,1]
	v_pk_mul_f32 v[38:39], v[34:35], v[26:27] op_sel_hi:[0,1]
	ds_read_b128 v[26:29], v163
	ds_read_b128 v[30:33], v164
	s_waitcnt lgkmcnt(0)
	v_pk_fma_f32 v[26:27], v[38:39], v[26:27], v[30:31]
	v_mov_b32_e32 v30, 0
	v_cvt_pk_fp8_f32 v30, v26, v27
	v_pk_fma_f32 v[28:29], v[36:37], v[28:29], v[32:33]
	v_pk_mul_f32 v[32:33], v[34:35], v[22:23] op_sel_hi:[0,1]
	v_cvt_pk_fp8_f32 v30, v28, v29 op_sel:[0,0,1]
	global_store_dword v[40:41], v30, off offset:256
	v_pk_mul_f32 v[30:31], v[34:35], v[24:25] op_sel_hi:[0,1]
	ds_read_b128 v[22:25], v165
	ds_read_b128 v[26:29], v166
	s_waitcnt lgkmcnt(0)
	v_pk_fma_f32 v[22:23], v[32:33], v[22:23], v[26:27]
	v_mov_b32_e32 v26, 0
	v_cvt_pk_fp8_f32 v26, v22, v23
	v_pk_fma_f32 v[24:25], v[30:31], v[24:25], v[28:29]
	v_pk_mul_f32 v[28:29], v[34:35], v[18:19] op_sel_hi:[0,1]
	v_cvt_pk_fp8_f32 v26, v24, v25 op_sel:[0,0,1]
	global_store_dword v[40:41], v26, off offset:512
	v_pk_mul_f32 v[26:27], v[34:35], v[20:21] op_sel_hi:[0,1]
	ds_read_b128 v[18:21], v167
	ds_read_b128 v[22:25], v168
	s_waitcnt lgkmcnt(0)
	v_pk_fma_f32 v[18:19], v[28:29], v[18:19], v[22:23]
	v_mov_b32_e32 v22, 0
	v_cvt_pk_fp8_f32 v22, v18, v19
	v_pk_fma_f32 v[20:21], v[26:27], v[20:21], v[24:25]
	v_pk_mul_f32 v[24:25], v[34:35], v[14:15] op_sel_hi:[0,1]
	v_cvt_pk_fp8_f32 v22, v20, v21 op_sel:[0,0,1]
	global_store_dword v[40:41], v22, off offset:768
	v_pk_mul_f32 v[22:23], v[34:35], v[16:17] op_sel_hi:[0,1]
	ds_read_b128 v[14:17], v169
	ds_read_b128 v[18:21], v170
	s_waitcnt lgkmcnt(0)
	v_pk_fma_f32 v[14:15], v[24:25], v[14:15], v[18:19]
	v_mov_b32_e32 v18, 0
	v_cvt_pk_fp8_f32 v18, v14, v15
	v_pk_fma_f32 v[16:17], v[22:23], v[16:17], v[20:21]
	v_pk_mul_f32 v[20:21], v[34:35], v[10:11] op_sel_hi:[0,1]
	v_cvt_pk_fp8_f32 v18, v16, v17 op_sel:[0,0,1]
	global_store_dword v[40:41], v18, off offset:1024
	v_pk_mul_f32 v[18:19], v[34:35], v[12:13] op_sel_hi:[0,1]
	ds_read_b128 v[10:13], v171
	ds_read_b128 v[14:17], v172
	s_waitcnt lgkmcnt(0)
	v_pk_fma_f32 v[10:11], v[20:21], v[10:11], v[14:15]
	v_mov_b32_e32 v14, 0
	v_cvt_pk_fp8_f32 v14, v10, v11
	v_pk_fma_f32 v[12:13], v[18:19], v[12:13], v[16:17]
	v_pk_mul_f32 v[16:17], v[34:35], v[6:7] op_sel_hi:[0,1]
	v_cvt_pk_fp8_f32 v14, v12, v13 op_sel:[0,0,1]
	global_store_dword v[40:41], v14, off offset:1280
	v_pk_mul_f32 v[14:15], v[34:35], v[8:9] op_sel_hi:[0,1]
	ds_read_b128 v[6:9], v173
	ds_read_b128 v[10:13], v174
	s_waitcnt lgkmcnt(0)
	v_pk_fma_f32 v[6:7], v[16:17], v[6:7], v[10:11]
	v_mov_b32_e32 v10, 0
	v_cvt_pk_fp8_f32 v10, v6, v7
	v_pk_fma_f32 v[8:9], v[14:15], v[8:9], v[12:13]
	v_pk_mul_f32 v[12:13], v[34:35], v[2:3] op_sel_hi:[0,1]
	v_cvt_pk_fp8_f32 v10, v8, v9 op_sel:[0,0,1]
	global_store_dword v[40:41], v10, off offset:1536
	v_pk_mul_f32 v[10:11], v[34:35], v[4:5] op_sel_hi:[0,1]
	ds_read_b128 v[2:5], v175
	ds_read_b128 v[6:9], v176
	s_waitcnt lgkmcnt(0)
	v_pk_fma_f32 v[2:3], v[12:13], v[2:3], v[6:7]
	v_mov_b32_e32 v6, 0
	v_cvt_pk_fp8_f32 v6, v2, v3
	v_pk_fma_f32 v[4:5], v[10:11], v[4:5], v[8:9]
	s_nop 0
	v_cvt_pk_fp8_f32 v6, v4, v5 op_sel:[0,0,1]
	v_or_b32_e32 v4, s65, v143
	v_ashrrev_i32_e32 v5, 31, v4
	v_lshl_add_u64 v[4:5], v[4:5], 2, s[54:55]
	global_store_dword v[40:41], v6, off offset:1792
	s_barrier
	global_load_dword v3, v[4:5], off
	global_load_dword v2, v[140:141], off
	v_readlane_b32 s54, v243, 12
	s_mulk_i32 s54, 0x410
	s_nop 0
	v_add_u32_e32 v4, s54, v158
	ds_read_b32 v5, v4 offset:1024
	ds_read_b32 v6, v4 offset:9344
	s_mov_b32 s54, 0xbfb8aa3b
	s_waitcnt lgkmcnt(1)
	v_add_f32_e32 v5, 0, v5
	s_waitcnt lgkmcnt(0)
	v_add_f32_e32 v5, v5, v6
	ds_read_b32 v6, v4 offset:17664
	s_waitcnt lgkmcnt(0)
	v_add_f32_e32 v5, v5, v6
	ds_read_b32 v6, v4 offset:25984
	s_waitcnt lgkmcnt(0)
	v_add_f32_e32 v5, v5, v6
	ds_read_b32 v6, v4 offset:34304
	s_waitcnt lgkmcnt(0)
	v_add_f32_e32 v5, v5, v6
	ds_read_b32 v6, v4 offset:42624
	s_waitcnt lgkmcnt(0)
	v_add_f32_e32 v5, v5, v6
	ds_read_b32 v6, v4 offset:50944
	s_waitcnt lgkmcnt(0)
	v_add_f32_e32 v5, v5, v6
	ds_read_b32 v6, v4 offset:59264
	s_waitcnt lgkmcnt(0)
	v_add_f32_e32 v5, v5, v6
	v_mov_b32_e32 v6, s64
	ds_read_b32 v6, v6
	s_waitcnt vmcnt(1) lgkmcnt(0)
	v_fma_f32 v5, v5, v6, v3
	v_mul_f32_e32 v6, 0xbfb8aa3b, v5
	v_fma_f32 v7, v5, s54, -v6
	v_rndne_f32_e32 v8, v6
	v_fmac_f32_e32 v7, 0xb2a5705f, v5
	v_sub_f32_e32 v6, v6, v8
	v_add_f32_e32 v6, v6, v7
	v_exp_f32_e32 v6, v6
	v_cvt_i32_f32_e32 v7, v8
	s_mov_b32 s54, 0x42ce8ed0
	v_cmp_nlt_f32_e32 vcc, s54, v5
	s_mov_b32 s54, 0xc2b17218
	v_ldexp_f32 v6, v6, v7
	v_cndmask_b32_e32 v6, 0, v6, vcc
	v_cmp_ngt_f32_e32 vcc, s54, v5
	s_nop 1
	v_cndmask_b32_e32 v5, v180, v6, vcc
	v_add_f32_e32 v5, 1.0, v5
	v_div_scale_f32 v6, s[54:55], v5, v5, 1.0
	v_rcp_f32_e32 v7, v6
	s_nop 0
	v_fma_f32 v8, -v6, v7, 1.0
	v_fmac_f32_e32 v7, v8, v7
	v_div_scale_f32 v8, vcc, 1.0, v5, 1.0
	v_mul_f32_e32 v9, v8, v7
	v_fma_f32 v10, -v6, v9, v8
	v_fmac_f32_e32 v9, v10, v7
	v_fma_f32 v6, -v6, v9, v8
	v_div_fmas_f32 v6, v6, v7, v9
	v_div_fixup_f32 v5, v6, v5, 1.0
	s_waitcnt vmcnt(0)
	v_add_f32_e32 v6, v2, v5
	s_nop 1
	v_mov_b32_dpp v7, v6 quad_perm:[1,0,3,2] row_mask:0xf bank_mask:0xf bound_ctrl:1
	v_max_f32_e32 v7, v7, v7
	v_max_f32_e32 v7, v6, v7
	s_nop 1
	v_mov_b32_dpp v8, v7 quad_perm:[2,3,0,1] row_mask:0xf bank_mask:0xf bound_ctrl:1
	v_max_f32_e32 v8, v8, v8
	v_max_f32_e32 v7, v7, v8
	s_nop 1
	v_mov_b32_dpp v8, v7 row_half_mirror row_mask:0xf bank_mask:0xf bound_ctrl:1
	v_max_f32_e32 v8, v8, v8
	v_max_f32_e32 v7, v7, v8
	v_cmp_eq_f32_e32 vcc, v6, v7
	s_nop 1
	v_cndmask_b32_e32 v8, 64, v143, vcc
	s_nop 1
	v_min_i32_dpp v8, v8, v8 quad_perm:[1,0,3,2] row_mask:0xf bank_mask:0xf bound_ctrl:1
	s_nop 1
	v_min_i32_dpp v8, v8, v8 quad_perm:[2,3,0,1] row_mask:0xf bank_mask:0xf bound_ctrl:1
	s_nop 1
	v_min_i32_dpp v8, v8, v8 row_half_mirror row_mask:0xf bank_mask:0xf bound_ctrl:1
	v_cmp_ne_u32_e32 vcc, v143, v8
	s_nop 1
	v_cndmask_b32_e32 v8, v181, v6, vcc
	s_nop 1
	v_mov_b32_dpp v9, v8 quad_perm:[1,0,3,2] row_mask:0xf bank_mask:0xf bound_ctrl:1
	v_max_f32_e32 v9, v9, v9
	v_max_f32_e32 v8, v8, v9
	s_nop 1
	v_mov_b32_dpp v9, v8 quad_perm:[2,3,0,1] row_mask:0xf bank_mask:0xf bound_ctrl:1
	v_max_f32_e32 v9, v9, v9
	v_max_f32_e32 v8, v8, v9
	s_nop 1
	v_mov_b32_dpp v9, v8 row_half_mirror row_mask:0xf bank_mask:0xf bound_ctrl:1
	v_max_f32_e32 v9, v9, v9
	v_max_f32_e32 v8, v8, v9
	v_add_f32_e32 v7, v7, v8
	s_nop 0
	v_readlane_b32 s54, v7, 0
	s_nop 1
	v_cmp_gt_f32_e32 vcc, s54, v7
	v_cmp_eq_f32_e64 s[54:55], s54, v7
	s_and_b64 s[54:55], s[54:55], s[6:7]
	s_or_b64 s[54:55], vcc, s[54:55]
	v_cndmask_b32_e64 v8, 0, 1, s[54:55]
	v_readlane_b32 s54, v7, 8
	s_nop 1
	v_cmp_gt_f32_e32 vcc, s54, v7
	v_cmp_eq_f32_e64 s[54:55], s54, v7
	s_and_b64 s[54:55], s[54:55], s[8:9]
	s_or_b64 s[54:55], vcc, s[54:55]
	v_cndmask_b32_e64 v9, 0, 1, s[54:55]
	v_readlane_b32 s54, v7, 16
	v_add_u32_e32 v8, v8, v9
	s_nop 0
	v_cmp_gt_f32_e32 vcc, s54, v7
	v_cmp_eq_f32_e64 s[54:55], s54, v7
	s_and_b64 s[54:55], s[54:55], s[10:11]
	s_or_b64 s[54:55], vcc, s[54:55]
	v_cndmask_b32_e64 v9, 0, 1, s[54:55]
	v_readlane_b32 s54, v7, 24
	s_nop 1
	v_cmp_gt_f32_e32 vcc, s54, v7
	v_cmp_eq_f32_e64 s[54:55], s54, v7
	s_and_b64 s[54:55], s[54:55], s[12:13]
	s_or_b64 s[54:55], vcc, s[54:55]
	v_cndmask_b32_e64 v10, 0, 1, s[54:55]
	v_readlane_b32 s54, v7, 32
	v_add3_u32 v8, v8, v9, v10
	s_nop 0
	v_cmp_gt_f32_e32 vcc, s54, v7
	v_cmp_eq_f32_e64 s[54:55], s54, v7
	s_and_b64 s[54:55], s[54:55], s[14:15]
	s_or_b64 s[54:55], vcc, s[54:55]
	v_cndmask_b32_e64 v9, 0, 1, s[54:55]
	v_readlane_b32 s54, v7, 40
	s_nop 1
	v_cmp_gt_f32_e32 vcc, s54, v7
	v_cmp_eq_f32_e64 s[54:55], s54, v7
	s_and_b64 s[54:55], s[54:55], s[16:17]
	s_or_b64 s[54:55], vcc, s[54:55]
	v_cndmask_b32_e64 v10, 0, 1, s[54:55]
	v_readlane_b32 s54, v7, 48
	v_add3_u32 v8, v8, v9, v10
	s_nop 0
	v_cmp_gt_f32_e32 vcc, s54, v7
	v_cmp_eq_f32_e64 s[54:55], s54, v7
	s_and_b64 s[54:55], s[54:55], s[66:67]
	s_or_b64 s[54:55], vcc, s[54:55]
	v_cndmask_b32_e64 v9, 0, 1, s[54:55]
	v_readlane_b32 s54, v7, 56
	v_readlane_b32 s66, v243, 40
	v_readlane_b32 s67, v243, 41
	v_cmp_gt_f32_e32 vcc, s54, v7
	s_nop 1
	v_addc_co_u32_e32 v7, vcc, v8, v9, vcc
	v_cmp_gt_u32_e32 vcc, 4, v7
	s_nop 1
	v_cndmask_b32_e32 v6, v181, v6, vcc
	s_nop 0
	v_readlane_b32 s54, v6, 0
	s_nop 1
	v_cmp_gt_f32_e32 vcc, s54, v6
	v_cmp_eq_f32_e64 s[54:55], s54, v6
	s_and_b64 s[54:55], s[54:55], s[66:67]
	s_or_b64 s[54:55], vcc, s[54:55]
	v_cndmask_b32_e64 v7, 0, 1, s[54:55]
	v_readlane_b32 s54, v6, 1
	v_readlane_b32 s66, v243, 42
	v_readlane_b32 s67, v243, 43
	v_cmp_gt_f32_e32 vcc, s54, v6
	v_cmp_eq_f32_e64 s[54:55], s54, v6
	s_and_b64 s[54:55], s[54:55], s[66:67]
	s_or_b64 s[54:55], vcc, s[54:55]
	v_cndmask_b32_e64 v8, 0, 1, s[54:55]
	v_readlane_b32 s54, v6, 2
	v_readlane_b32 s66, v243, 44
	v_readlane_b32 s67, v243, 45
	v_cmp_gt_f32_e32 vcc, s54, v6
	v_cmp_eq_f32_e64 s[54:55], s54, v6
	s_and_b64 s[54:55], s[54:55], s[66:67]
	s_or_b64 s[54:55], vcc, s[54:55]
	v_add_u32_e32 v7, v7, v8
	v_cndmask_b32_e64 v8, 0, 1, s[54:55]
	v_readlane_b32 s54, v6, 3
	v_readlane_b32 s66, v243, 46
	v_readlane_b32 s67, v243, 47
	v_cmp_gt_f32_e32 vcc, s54, v6
	v_cmp_eq_f32_e64 s[54:55], s54, v6
	s_and_b64 s[54:55], s[54:55], s[66:67]
	s_or_b64 s[54:55], vcc, s[54:55]
	v_cndmask_b32_e64 v9, 0, 1, s[54:55]
	v_readlane_b32 s54, v6, 4
	v_readlane_b32 s66, v243, 48
	v_readlane_b32 s67, v243, 49
	v_cmp_gt_f32_e32 vcc, s54, v6
	v_cmp_eq_f32_e64 s[54:55], s54, v6
	s_and_b64 s[54:55], s[54:55], s[66:67]
	s_or_b64 s[54:55], vcc, s[54:55]
	v_add3_u32 v7, v7, v8, v9
	v_cndmask_b32_e64 v8, 0, 1, s[54:55]
	v_readlane_b32 s54, v6, 5
	v_readlane_b32 s66, v243, 50
	v_readlane_b32 s67, v243, 51
	v_cmp_gt_f32_e32 vcc, s54, v6
	v_cmp_eq_f32_e64 s[54:55], s54, v6
	s_and_b64 s[54:55], s[54:55], s[66:67]
	s_or_b64 s[54:55], vcc, s[54:55]
	v_cndmask_b32_e64 v9, 0, 1, s[54:55]
	v_readlane_b32 s54, v6, 6
	v_readlane_b32 s66, v243, 52
	v_readlane_b32 s67, v243, 53
	v_cmp_gt_f32_e32 vcc, s54, v6
	v_cmp_eq_f32_e64 s[54:55], s54, v6
	s_and_b64 s[54:55], s[54:55], s[66:67]
	s_or_b64 s[54:55], vcc, s[54:55]
	v_add3_u32 v7, v7, v8, v9
	v_cndmask_b32_e64 v8, 0, 1, s[54:55]
	v_readlane_b32 s54, v6, 7
	v_readlane_b32 s66, v243, 54
	v_readlane_b32 s67, v243, 55
	v_cmp_gt_f32_e32 vcc, s54, v6
	v_cmp_eq_f32_e64 s[54:55], s54, v6
	s_and_b64 s[54:55], s[54:55], s[6:7]
	s_or_b64 s[54:55], vcc, s[54:55]
	v_cndmask_b32_e64 v9, 0, 1, s[54:55]
	v_readlane_b32 s54, v6, 8
	v_add3_u32 v7, v7, v8, v9
	s_nop 0
	v_cmp_gt_f32_e32 vcc, s54, v6
	v_cmp_eq_f32_e64 s[54:55], s54, v6
	s_and_b64 s[54:55], s[54:55], s[66:67]
	s_or_b64 s[54:55], vcc, s[54:55]
	v_cndmask_b32_e64 v8, 0, 1, s[54:55]
	v_readlane_b32 s54, v6, 9
	v_readlane_b32 s66, v243, 56
	v_readlane_b32 s67, v243, 57
	v_cmp_gt_f32_e32 vcc, s54, v6
	v_cmp_eq_f32_e64 s[54:55], s54, v6
	s_and_b64 s[54:55], s[54:55], s[66:67]
	s_or_b64 s[54:55], vcc, s[54:55]
	v_cndmask_b32_e64 v9, 0, 1, s[54:55]
	v_readlane_b32 s54, v6, 10
	v_readlane_b32 s66, v243, 58
	v_readlane_b32 s67, v243, 59
	v_cmp_gt_f32_e32 vcc, s54, v6
	v_cmp_eq_f32_e64 s[54:55], s54, v6
	s_and_b64 s[54:55], s[54:55], s[66:67]
	s_or_b64 s[54:55], vcc, s[54:55]
	v_add3_u32 v7, v7, v8, v9
	v_cndmask_b32_e64 v8, 0, 1, s[54:55]
	v_readlane_b32 s54, v6, 11
	v_readlane_b32 s66, v243, 60
	v_readlane_b32 s67, v243, 61
	v_cmp_gt_f32_e32 vcc, s54, v6
	v_cmp_eq_f32_e64 s[54:55], s54, v6
	s_and_b64 s[54:55], s[54:55], s[66:67]
	s_or_b64 s[54:55], vcc, s[54:55]
	v_cndmask_b32_e64 v9, 0, 1, s[54:55]
	v_readlane_b32 s54, v6, 12
	v_readlane_b32 s66, v243, 62
	v_readlane_b32 s67, v243, 63
	v_cmp_gt_f32_e32 vcc, s54, v6
	v_cmp_eq_f32_e64 s[54:55], s54, v6
	s_and_b64 s[54:55], s[54:55], s[66:67]
	s_or_b64 s[54:55], vcc, s[54:55]
	v_add3_u32 v7, v7, v8, v9
	v_cndmask_b32_e64 v8, 0, 1, s[54:55]
	v_readlane_b32 s54, v6, 13
	v_readlane_b32 s66, v242, 0
	v_readlane_b32 s67, v242, 1
	v_cmp_gt_f32_e32 vcc, s54, v6
	v_cmp_eq_f32_e64 s[54:55], s54, v6
	s_and_b64 s[54:55], s[54:55], s[66:67]
	s_or_b64 s[54:55], vcc, s[54:55]
	v_cndmask_b32_e64 v9, 0, 1, s[54:55]
	v_readlane_b32 s54, v6, 14
	v_readlane_b32 s66, v242, 2
	v_readlane_b32 s67, v242, 3
	v_cmp_gt_f32_e32 vcc, s54, v6
	v_cmp_eq_f32_e64 s[54:55], s54, v6
	s_and_b64 s[54:55], s[54:55], s[66:67]
	s_or_b64 s[54:55], vcc, s[54:55]
	v_add3_u32 v7, v7, v8, v9
	v_cndmask_b32_e64 v8, 0, 1, s[54:55]
	v_readlane_b32 s54, v6, 15
	v_readlane_b32 s66, v242, 4
	v_readlane_b32 s67, v242, 5
	v_cmp_gt_f32_e32 vcc, s54, v6
	v_cmp_eq_f32_e64 s[54:55], s54, v6
	s_and_b64 s[54:55], s[54:55], s[8:9]
	s_or_b64 s[54:55], vcc, s[54:55]
	v_cndmask_b32_e64 v9, 0, 1, s[54:55]
	v_readlane_b32 s54, v6, 16
	v_add3_u32 v7, v7, v8, v9
	s_nop 0
	v_cmp_gt_f32_e32 vcc, s54, v6
	v_cmp_eq_f32_e64 s[54:55], s54, v6
	s_and_b64 s[54:55], s[54:55], s[66:67]
	s_or_b64 s[54:55], vcc, s[54:55]
	v_cndmask_b32_e64 v8, 0, 1, s[54:55]
	v_readlane_b32 s54, v6, 17
	v_readlane_b32 s66, v242, 6
	v_readlane_b32 s67, v242, 7
	v_cmp_gt_f32_e32 vcc, s54, v6
	v_cmp_eq_f32_e64 s[54:55], s54, v6
	s_and_b64 s[54:55], s[54:55], s[66:67]
	s_or_b64 s[54:55], vcc, s[54:55]
	v_cndmask_b32_e64 v9, 0, 1, s[54:55]
	v_readlane_b32 s54, v6, 18
	v_readlane_b32 s66, v242, 8
	v_readlane_b32 s67, v242, 9
	v_cmp_gt_f32_e32 vcc, s54, v6
	v_cmp_eq_f32_e64 s[54:55], s54, v6
	s_and_b64 s[54:55], s[54:55], s[66:67]
	s_or_b64 s[54:55], vcc, s[54:55]
	v_add3_u32 v7, v7, v8, v9
	v_cndmask_b32_e64 v8, 0, 1, s[54:55]
	v_readlane_b32 s54, v6, 19
	v_readlane_b32 s66, v242, 10
	v_readlane_b32 s67, v242, 11
	v_cmp_gt_f32_e32 vcc, s54, v6
	v_cmp_eq_f32_e64 s[54:55], s54, v6
	s_and_b64 s[54:55], s[54:55], s[66:67]
	s_or_b64 s[54:55], vcc, s[54:55]
	v_cndmask_b32_e64 v9, 0, 1, s[54:55]
	v_readlane_b32 s54, v6, 20
	v_readlane_b32 s66, v242, 12
	v_readlane_b32 s67, v242, 13
	v_cmp_gt_f32_e32 vcc, s54, v6
	v_cmp_eq_f32_e64 s[54:55], s54, v6
	s_and_b64 s[54:55], s[54:55], s[66:67]
	s_or_b64 s[54:55], vcc, s[54:55]
	v_add3_u32 v7, v7, v8, v9
	v_cndmask_b32_e64 v8, 0, 1, s[54:55]
	v_readlane_b32 s54, v6, 21
	v_readlane_b32 s66, v242, 14
	v_readlane_b32 s67, v242, 15
	v_cmp_gt_f32_e32 vcc, s54, v6
	v_cmp_eq_f32_e64 s[54:55], s54, v6
	s_and_b64 s[54:55], s[54:55], s[66:67]
	s_or_b64 s[54:55], vcc, s[54:55]
	v_cndmask_b32_e64 v9, 0, 1, s[54:55]
	v_readlane_b32 s54, v6, 22
	v_readlane_b32 s66, v242, 16
	v_readlane_b32 s67, v242, 17
	v_cmp_gt_f32_e32 vcc, s54, v6
	v_cmp_eq_f32_e64 s[54:55], s54, v6
	s_and_b64 s[54:55], s[54:55], s[66:67]
	s_or_b64 s[54:55], vcc, s[54:55]
	v_add3_u32 v7, v7, v8, v9
	v_cndmask_b32_e64 v8, 0, 1, s[54:55]
	v_readlane_b32 s54, v6, 23
	v_readlane_b32 s66, v242, 18
	v_readlane_b32 s67, v242, 19
	v_cmp_gt_f32_e32 vcc, s54, v6
	v_cmp_eq_f32_e64 s[54:55], s54, v6
	s_and_b64 s[54:55], s[54:55], s[10:11]
	s_or_b64 s[54:55], vcc, s[54:55]
	v_cndmask_b32_e64 v9, 0, 1, s[54:55]
	v_readlane_b32 s54, v6, 24
	v_add3_u32 v7, v7, v8, v9
	s_nop 0
	v_cmp_gt_f32_e32 vcc, s54, v6
	v_cmp_eq_f32_e64 s[54:55], s54, v6
	s_and_b64 s[54:55], s[54:55], s[66:67]
	s_or_b64 s[54:55], vcc, s[54:55]
	v_cndmask_b32_e64 v8, 0, 1, s[54:55]
	v_readlane_b32 s54, v6, 25
	v_readlane_b32 s66, v242, 25
	v_readlane_b32 s67, v242, 26
	v_cmp_gt_f32_e32 vcc, s54, v6
	v_cmp_eq_f32_e64 s[54:55], s54, v6
	s_and_b64 s[54:55], s[54:55], s[66:67]
	s_or_b64 s[54:55], vcc, s[54:55]
	v_cndmask_b32_e64 v9, 0, 1, s[54:55]
	v_readlane_b32 s54, v6, 26
	v_add3_u32 v7, v7, v8, v9
	s_nop 0
	v_cmp_gt_f32_e32 vcc, s54, v6
	v_cmp_eq_f32_e64 s[54:55], s54, v6
	s_and_b64 s[54:55], s[54:55], s[68:69]
	s_or_b64 s[54:55], vcc, s[54:55]
	v_cndmask_b32_e64 v8, 0, 1, s[54:55]
	v_readlane_b32 s54, v6, 27
	s_nop 1
	v_cmp_gt_f32_e32 vcc, s54, v6
	v_cmp_eq_f32_e64 s[54:55], s54, v6
	s_and_b64 s[54:55], s[54:55], s[70:71]
	s_or_b64 s[54:55], vcc, s[54:55]
	v_cndmask_b32_e64 v9, 0, 1, s[54:55]
	v_readlane_b32 s54, v6, 28
	v_add3_u32 v7, v7, v8, v9
	s_nop 0
	v_cmp_gt_f32_e32 vcc, s54, v6
	v_cmp_eq_f32_e64 s[54:55], s54, v6
	s_and_b64 s[54:55], s[54:55], s[72:73]
	s_or_b64 s[54:55], vcc, s[54:55]
	v_cndmask_b32_e64 v8, 0, 1, s[54:55]
	v_readlane_b32 s54, v6, 29
	s_nop 1
	v_cmp_gt_f32_e32 vcc, s54, v6
	v_cmp_eq_f32_e64 s[54:55], s54, v6
	s_and_b64 s[54:55], s[54:55], s[74:75]
	s_or_b64 s[54:55], vcc, s[54:55]
	v_cndmask_b32_e64 v9, 0, 1, s[54:55]
	v_readlane_b32 s54, v6, 30
	v_add3_u32 v7, v7, v8, v9
	s_nop 0
	v_cmp_gt_f32_e32 vcc, s54, v6
	v_cmp_eq_f32_e64 s[54:55], s54, v6
	s_and_b64 s[54:55], s[54:55], s[76:77]
	s_or_b64 s[54:55], vcc, s[54:55]
	v_cndmask_b32_e64 v8, 0, 1, s[54:55]
	v_readlane_b32 s54, v6, 31
	s_nop 1
	v_cmp_gt_f32_e32 vcc, s54, v6
	v_cmp_eq_f32_e64 s[54:55], s54, v6
	s_and_b64 s[54:55], s[54:55], s[12:13]
	s_or_b64 s[54:55], vcc, s[54:55]
	v_cndmask_b32_e64 v9, 0, 1, s[54:55]
	v_readlane_b32 s54, v6, 32
	v_add3_u32 v7, v7, v8, v9
	s_nop 0
	v_cmp_gt_f32_e32 vcc, s54, v6
	v_cmp_eq_f32_e64 s[54:55], s54, v6
	s_and_b64 s[54:55], s[54:55], s[78:79]
	s_or_b64 s[54:55], vcc, s[54:55]
	v_cndmask_b32_e64 v8, 0, 1, s[54:55]
	v_readlane_b32 s54, v6, 33
	s_nop 1
	v_cmp_gt_f32_e32 vcc, s54, v6
	v_cmp_eq_f32_e64 s[54:55], s54, v6
	s_and_b64 s[54:55], s[54:55], s[80:81]
	s_or_b64 s[54:55], vcc, s[54:55]
	v_cndmask_b32_e64 v9, 0, 1, s[54:55]
	v_readlane_b32 s54, v6, 34
	v_add3_u32 v7, v7, v8, v9
	s_nop 0
	v_cmp_gt_f32_e32 vcc, s54, v6
	v_cmp_eq_f32_e64 s[54:55], s54, v6
	s_and_b64 s[54:55], s[54:55], s[82:83]
	s_or_b64 s[54:55], vcc, s[54:55]
	v_cndmask_b32_e64 v8, 0, 1, s[54:55]
	v_readlane_b32 s54, v6, 35
	s_nop 1
	v_cmp_gt_f32_e32 vcc, s54, v6
	v_cmp_eq_f32_e64 s[54:55], s54, v6
	s_and_b64 s[54:55], s[54:55], s[84:85]
	s_or_b64 s[54:55], vcc, s[54:55]
	v_cndmask_b32_e64 v9, 0, 1, s[54:55]
	v_readlane_b32 s54, v6, 36
	v_add3_u32 v7, v7, v8, v9
	s_nop 0
	v_cmp_gt_f32_e32 vcc, s54, v6
	v_cmp_eq_f32_e64 s[54:55], s54, v6
	s_and_b64 s[54:55], s[54:55], s[86:87]
	s_or_b64 s[54:55], vcc, s[54:55]
	v_cndmask_b32_e64 v8, 0, 1, s[54:55]
	v_readlane_b32 s54, v6, 37
	s_nop 1
	v_cmp_gt_f32_e32 vcc, s54, v6
	v_cmp_eq_f32_e64 s[54:55], s54, v6
	s_and_b64 s[54:55], s[54:55], s[88:89]
	s_or_b64 s[54:55], vcc, s[54:55]
	v_cndmask_b32_e64 v9, 0, 1, s[54:55]
	v_readlane_b32 s54, v6, 38
	v_add3_u32 v7, v7, v8, v9
	s_nop 0
	v_cmp_gt_f32_e32 vcc, s54, v6
	v_cmp_eq_f32_e64 s[54:55], s54, v6
	s_and_b64 s[54:55], s[54:55], s[90:91]
	s_or_b64 s[54:55], vcc, s[54:55]
	v_cndmask_b32_e64 v8, 0, 1, s[54:55]
	v_readlane_b32 s54, v6, 39
	s_nop 1
	v_cmp_gt_f32_e32 vcc, s54, v6
	v_cmp_eq_f32_e64 s[54:55], s54, v6
	s_and_b64 s[54:55], s[54:55], s[14:15]
	s_or_b64 s[54:55], vcc, s[54:55]
	v_cndmask_b32_e64 v9, 0, 1, s[54:55]
	v_readlane_b32 s54, v6, 40
	v_add3_u32 v7, v7, v8, v9
	s_nop 0
	v_cmp_gt_f32_e32 vcc, s54, v6
	v_cmp_eq_f32_e64 s[54:55], s54, v6
	s_and_b64 s[54:55], s[54:55], s[92:93]
	s_or_b64 s[54:55], vcc, s[54:55]
	v_cndmask_b32_e64 v8, 0, 1, s[54:55]
	v_readlane_b32 s54, v6, 41
	s_nop 1
	v_cmp_gt_f32_e32 vcc, s54, v6
	v_cmp_eq_f32_e64 s[54:55], s54, v6
	s_and_b64 s[54:55], s[54:55], s[94:95]
	s_or_b64 s[54:55], vcc, s[54:55]
	v_cndmask_b32_e64 v9, 0, 1, s[54:55]
	v_readlane_b32 s54, v6, 42
	v_add3_u32 v7, v7, v8, v9
	s_nop 0
	v_cmp_gt_f32_e32 vcc, s54, v6
	v_cmp_eq_f32_e64 s[54:55], s54, v6
	s_and_b64 s[54:55], s[54:55], s[96:97]
	s_or_b64 s[54:55], vcc, s[54:55]
	v_cndmask_b32_e64 v8, 0, 1, s[54:55]
	v_readlane_b32 s54, v6, 43
	s_nop 1
	v_cmp_gt_f32_e32 vcc, s54, v6
	v_cmp_eq_f32_e64 s[54:55], s54, v6
	s_and_b64 s[54:55], s[54:55], s[52:53]
	s_or_b64 s[54:55], vcc, s[54:55]
	v_cndmask_b32_e64 v9, 0, 1, s[54:55]
	v_readlane_b32 s54, v6, 44
	v_add3_u32 v7, v7, v8, v9
	s_nop 0
	v_cmp_gt_f32_e32 vcc, s54, v6
	v_cmp_eq_f32_e64 s[54:55], s54, v6
	s_and_b64 s[54:55], s[54:55], s[0:1]
	s_or_b64 s[54:55], vcc, s[54:55]
	v_cndmask_b32_e64 v8, 0, 1, s[54:55]
	v_readlane_b32 s54, v6, 45
	s_nop 1
	v_cmp_gt_f32_e32 vcc, s54, v6
	v_cmp_eq_f32_e64 s[54:55], s54, v6
	s_and_b64 s[54:55], s[54:55], s[4:5]
	s_or_b64 s[54:55], vcc, s[54:55]
	v_cndmask_b32_e64 v9, 0, 1, s[54:55]
	v_readlane_b32 s54, v6, 46
	v_add3_u32 v7, v7, v8, v9
	s_nop 0
	v_cmp_gt_f32_e32 vcc, s54, v6
	v_cmp_eq_f32_e64 s[54:55], s54, v6
	s_and_b64 s[54:55], s[54:55], s[18:19]
	s_or_b64 s[54:55], vcc, s[54:55]
	v_cndmask_b32_e64 v8, 0, 1, s[54:55]
	v_readlane_b32 s54, v6, 47
	s_nop 1
	v_cmp_gt_f32_e32 vcc, s54, v6
	v_cmp_eq_f32_e64 s[54:55], s54, v6
	s_and_b64 s[54:55], s[54:55], s[16:17]
	s_or_b64 s[54:55], vcc, s[54:55]
	v_cndmask_b32_e64 v9, 0, 1, s[54:55]
	v_readlane_b32 s54, v6, 48
	v_add3_u32 v7, v7, v8, v9
	s_nop 0
	v_cmp_gt_f32_e32 vcc, s54, v6
	v_cmp_eq_f32_e64 s[54:55], s54, v6
	s_and_b64 s[54:55], s[54:55], s[20:21]
	s_or_b64 s[54:55], vcc, s[54:55]
	v_cndmask_b32_e64 v8, 0, 1, s[54:55]
	v_readlane_b32 s54, v6, 49
	s_nop 1
	v_cmp_gt_f32_e32 vcc, s54, v6
	v_cmp_eq_f32_e64 s[54:55], s54, v6
	s_and_b64 s[54:55], s[54:55], s[22:23]
	s_or_b64 s[54:55], vcc, s[54:55]
	v_cndmask_b32_e64 v9, 0, 1, s[54:55]
	v_readlane_b32 s54, v6, 50
	v_add3_u32 v7, v7, v8, v9
	s_nop 0
	v_cmp_gt_f32_e32 vcc, s54, v6
	v_cmp_eq_f32_e64 s[54:55], s54, v6
	s_and_b64 s[54:55], s[54:55], s[24:25]
	s_or_b64 s[54:55], vcc, s[54:55]
	v_cndmask_b32_e64 v8, 0, 1, s[54:55]
	v_readlane_b32 s54, v6, 51
	s_nop 1
	v_cmp_gt_f32_e32 vcc, s54, v6
	v_cmp_eq_f32_e64 s[54:55], s54, v6
	s_and_b64 s[54:55], s[54:55], s[26:27]
	s_or_b64 s[54:55], vcc, s[54:55]
	v_cndmask_b32_e64 v9, 0, 1, s[54:55]
	v_readlane_b32 s54, v6, 52
	v_add3_u32 v7, v7, v8, v9
	s_nop 0
	v_cmp_gt_f32_e32 vcc, s54, v6
	v_cmp_eq_f32_e64 s[54:55], s54, v6
	s_and_b64 s[54:55], s[54:55], s[28:29]
	s_or_b64 s[54:55], vcc, s[54:55]
	v_cndmask_b32_e64 v8, 0, 1, s[54:55]
	v_readlane_b32 s54, v6, 53
	s_nop 1
	v_cmp_gt_f32_e32 vcc, s54, v6
	v_cmp_eq_f32_e64 s[54:55], s54, v6
	s_and_b64 s[54:55], s[54:55], s[30:31]
	s_or_b64 s[54:55], vcc, s[54:55]
	v_cndmask_b32_e64 v9, 0, 1, s[54:55]
	v_readlane_b32 s54, v6, 54
	v_add3_u32 v7, v7, v8, v9
	s_nop 0
	v_cmp_gt_f32_e32 vcc, s54, v6
	v_cmp_eq_f32_e64 s[54:55], s54, v6
	s_and_b64 s[54:55], s[54:55], s[34:35]
	s_or_b64 s[54:55], vcc, s[54:55]
	v_cndmask_b32_e64 v8, 0, 1, s[54:55]
	v_readlane_b32 s54, v6, 55
	s_nop 1
	v_cmp_gt_f32_e32 vcc, s54, v6
	v_cmp_eq_f32_e64 s[54:55], s54, v6
	s_and_b64 s[54:55], s[54:55], s[36:37]
	s_or_b64 s[54:55], vcc, s[54:55]
	v_cndmask_b32_e64 v9, 0, 1, s[54:55]
	v_readlane_b32 s54, v6, 56
	v_add3_u32 v7, v7, v8, v9
	s_nop 0
	v_cmp_gt_f32_e32 vcc, s54, v6
	v_cmp_eq_f32_e64 s[54:55], s54, v6
	s_and_b64 s[54:55], s[54:55], s[38:39]
	s_or_b64 s[54:55], vcc, s[54:55]
	v_cndmask_b32_e64 v8, 0, 1, s[54:55]
	v_readlane_b32 s54, v6, 57
	s_nop 1
	v_cmp_gt_f32_e32 vcc, s54, v6
	v_cmp_eq_f32_e64 s[54:55], s54, v6
	s_and_b64 s[54:55], s[54:55], s[40:41]
	s_or_b64 s[54:55], vcc, s[54:55]
	v_cndmask_b32_e64 v9, 0, 1, s[54:55]
	v_readlane_b32 s54, v6, 58
	v_add3_u32 v7, v7, v8, v9
	s_nop 0
	v_cmp_gt_f32_e32 vcc, s54, v6
	v_cmp_eq_f32_e64 s[54:55], s54, v6
	s_and_b64 s[54:55], s[54:55], s[42:43]
	s_or_b64 s[54:55], vcc, s[54:55]
	v_cndmask_b32_e64 v8, 0, 1, s[54:55]
	v_readlane_b32 s54, v6, 59
	s_nop 1
	v_cmp_gt_f32_e32 vcc, s54, v6
	v_cmp_eq_f32_e64 s[54:55], s54, v6
	s_and_b64 s[54:55], s[54:55], s[44:45]
	s_or_b64 s[54:55], vcc, s[54:55]
	v_cndmask_b32_e64 v9, 0, 1, s[54:55]
	v_readlane_b32 s54, v6, 60
	v_add3_u32 v7, v7, v8, v9
	s_nop 0
	v_cmp_gt_f32_e32 vcc, s54, v6
	v_cmp_eq_f32_e64 s[54:55], s54, v6
	s_and_b64 s[54:55], s[54:55], s[46:47]
	s_or_b64 s[54:55], vcc, s[54:55]
	v_cndmask_b32_e64 v8, 0, 1, s[54:55]
	v_readlane_b32 s54, v6, 61
	s_nop 1
	v_cmp_gt_f32_e32 vcc, s54, v6
	v_cmp_eq_f32_e64 s[54:55], s54, v6
	s_and_b64 s[54:55], s[54:55], s[48:49]
	s_or_b64 s[54:55], vcc, s[54:55]
	v_cndmask_b32_e64 v9, 0, 1, s[54:55]
	v_readlane_b32 s54, v6, 62
	v_add3_u32 v7, v7, v8, v9
	s_nop 0
	v_cmp_gt_f32_e32 vcc, s54, v6
	v_cmp_eq_f32_e64 s[54:55], s54, v6
	s_and_b64 s[54:55], s[54:55], s[50:51]
	s_or_b64 s[54:55], vcc, s[54:55]
	v_cndmask_b32_e64 v8, 0, 1, s[54:55]
	v_readlane_b32 s54, v6, 63
	s_nop 1
	v_cmp_gt_f32_e32 vcc, s54, v6
	s_nop 1
	v_addc_co_u32_e32 v6, vcc, v7, v8, vcc
	v_cmp_gt_u32_e32 vcc, 8, v6
	s_nop 1
	v_cndmask_b32_e32 v6, 0, v5, vcc
	ds_swizzle_b32 v7, v6 offset:swizzle(SWAP,1)
	s_waitcnt lgkmcnt(0)
	v_add_f32_e32 v6, v6, v7
	ds_swizzle_b32 v7, v6 offset:swizzle(SWAP,2)
	s_waitcnt lgkmcnt(0)
	v_add_f32_e32 v6, v6, v7
	ds_swizzle_b32 v7, v6 offset:swizzle(SWAP,4)
	s_waitcnt lgkmcnt(0)
	v_add_f32_e32 v6, v6, v7
	ds_swizzle_b32 v7, v6 offset:swizzle(SWAP,8)
	s_waitcnt lgkmcnt(0)
	v_add_f32_e32 v6, v6, v7
	ds_swizzle_b32 v7, v6 offset:swizzle(SWAP,16)
	s_waitcnt lgkmcnt(0)
	v_add_f32_e32 v6, v6, v7
	v_mov_b32_e32 v7, v6
	s_nop 1
	v_permlane32_swap_b32_e32 v6, v7
	s_and_saveexec_b64 s[54:55], vcc
	s_cbranch_execz .LBB0_836
	v_add_f32_e32 v10, v6, v7
	ds_add_rtn_u32 v6, v158, v179 offset:512
	v_and_b32_e32 v8, vcc_lo, v142
	v_and_b32_e32 v7, vcc_hi, v1
	v_bcnt_u32_b32 v8, v8, 0
	v_bcnt_u32_b32 v132, v7, v8
	s_waitcnt lgkmcnt(0)
	v_or_b32_e32 v11, v6, v159
	v_lshl_add_u64 v[6:7], s[62:63], 3, v[132:133]
	v_div_scale_f32 v12, s[62:63], v10, v10, v5
	v_rcp_f32_e32 v13, v12
	v_readlane_b32 s62, v243, 28
	v_lshlrev_b64 v[6:7], 2, v[6:7]
	v_readlane_b32 s63, v243, 29
	s_nop 1
	v_lshl_add_u64 v[8:9], s[62:63], 0, v[6:7]
	global_store_dword v[8:9], v11, off
	v_fma_f32 v8, -v12, v13, 1.0
	v_fmac_f32_e32 v13, v8, v13
	v_div_scale_f32 v8, vcc, v5, v10, v5
	v_mul_f32_e32 v9, v8, v13
	v_fma_f32 v11, -v12, v9, v8
	v_fmac_f32_e32 v9, v11, v13
	v_fma_f32 v8, -v12, v9, v8
	v_div_fmas_f32 v8, v8, v13, v9
	v_readlane_b32 s62, v243, 30
	v_div_fixup_f32 v5, v8, v10, v5
	v_readlane_b32 s63, v243, 31
	v_mul_f32_e32 v5, 0x40200000, v5
	s_nop 0
	v_lshl_add_u64 v[6:7], s[62:63], 0, v[6:7]
	global_store_dword v[6:7], v5, off
